# s_setprio flips removed from GEMM loops (second paired run)
# speedup vs baseline: 1.0306x; 1.0075x over previous
; #define PG8_STAGE_A(bufoff, base_, nx_, kb_, h_) do { if (GATHER) { if (nx_) PG8_STAGE_G(bufoff, kb_, goN, h_); else PG8_STAGE_G(bufoff, kb_, goC, h_); } \
;         else PG8_STAGE(bufoff, (base_) + (kb_) + (h_) * hstep, voffA); } while (0)
; #define PG8_STAGE(bufoff, gbase, voff) do { _Pragma("unroll") for (int _i = 0; _i < 2; ++_i) \
;         __builtin_amdgcn_global_load_lds((const unsigned*)((const char*)(gbase) + (voff)[_i]), (LAS unsigned*)(lds + (bufoff) + ldsw + _i * 8192), 16, 0, 0); } while (0)
; #define PG8_LDA(dst, b, h) do { _Pragma("unroll") for (int m = 0; m < 4; ++m) _Pragma("unroll") for (int k = 0; k < 2; ++k) dst[m][k] = *(const LAS bf16x8*)(lds + PG8_SA(b, h) + aoff + m * 2048 + k * 1024); } while (0)
; #define PG8_LDB(dst, b, h) do { _Pragma("unroll") for (int n = 0; n < 2; ++n) _Pragma("unroll") for (int k = 0; k < 2; ++k) dst[n][k] = *(const LAS bf16x8*)(lds + PG8_SB(b, h) + boff + n * 2048 + k * 1024); } while (0)
; #define PG8_MMA(ai, bj, At, Bt) do { __builtin_amdgcn_s_setprio(1); _Pragma("unroll") for (int m = 0; m < 4; ++m) _Pragma("unroll") for (int n = 0; n < 2; ++n) _Pragma("unroll") for (int k = 0; k < 2; ++k) \
;         acc[ai][bj][m][n] = __builtin_amdgcn_mfma_f32_16x16x32_bf16(Bt[n][k], At[m][k], acc[ai][bj][m][n], 0, 0, 0); __builtin_amdgcn_s_setprio(0); } while (0)
; #define PG8_WAIT_V(n) asm volatile("s_waitcnt vmcnt(" #n ")" ::: "memory")
; #define PG8_WAIT_L(n) asm volatile("s_waitcnt lgkmcnt(" #n ")" ::: "memory")
; #define PG8_BAR __builtin_amdgcn_s_barrier()
; #define PG8_SCHED __builtin_amdgcn_sched_barrier(0)
; template <class Epi, class Sched, bool GATHER = false>
; __device__ __forceinline__ void gemm_phase(LAS unsigned char* lds, const Gemm g, const Sched& S, const Epi& E, const int tid) {
;     ...
;             PG8_LDB(B0, 0, 0); PG8_LDB(B1, 0, 1); PG8_SCHED; PG8_LDA(At, 0, 0); PG8_STAGE_A(PG8_SA(1, 1), cA, false, kb1, 1);
;             PG8_WAIT_V(8); PG8_WAIT_L(0); PG8_BAR; PG8_MMA(0, 0, At, B0); PG8_MMA(0, 1, At, B1); PG8_BAR; PG8_SCHED;
;             PG8_LDA(At, 0, 1); PG8_STAGE(PG8_SB(0, 0), b2, voffB); PG8_STAGE(PG8_SB(0, 1), b2 + hstep, voffB); PG8_STAGE_A(PG8_SA(0, 0), (last ? nA : cA), last, kb2, 0);
;             PG8_WAIT_V(8); PG8_WAIT_L(0); PG8_BAR; PG8_MMA(1, 0, At, B0); PG8_MMA(1, 1, At, B1); PG8_BAR; PG8_SCHED;
.LBB0_247:
	s_add_u32 s22, s28, 0x100
	s_addc_u32 s23, s29, 0
	s_add_u32 s54, s49, s28
	s_addc_u32 s55, s50, s29
	s_add_i32 s24, 0, 0x10000
	s_add_i32 s56, 0, 0x14000
	v_add_u32_e32 v2, s24, v1
	ds_read_b128 v[152:155], v2
	ds_read_b128 v[156:159], v2 offset:1024
	ds_read_b128 v[160:163], v2 offset:2048
	ds_read_b128 v[164:167], v2 offset:3072
	v_add_u32_e32 v2, s56, v1
	ds_read_b128 v[168:171], v2
	ds_read_b128 v[172:175], v2 offset:1024
	ds_read_b128 v[176:179], v2 offset:2048
	ds_read_b128 v[180:183], v2 offset:3072
	s_add_i32 s58, s24, s38
	s_add_i32 m0, s11, 0xc000
	s_add_i32 s57, s11, 0xe000
	s_add_i32 s59, s58, 0x2000
	s_cmp_eq_u32 s51, 28
	s_cselect_b64 s[52:53], -1, 0
	s_and_b64 s[24:25], s[52:53], exec
	s_cselect_b32 s25, s13, s55
	s_cselect_b32 s24, s15, s54
	v_lshl_add_u64 v[218:219], v[4:5], 0, s[28:29]
	ds_read_b128 v[184:187], v150
	ds_read_b128 v[188:191], v150 offset:1024
	ds_read_b128 v[192:195], v150 offset:2048
	ds_read_b128 v[196:199], v150 offset:3072
	ds_read_b128 v[202:205], v150 offset:4096
	ds_read_b128 v[206:209], v150 offset:5120
	ds_read_b128 v[210:213], v150 offset:6144
	ds_read_b128 v[214:217], v150 offset:7168
	global_load_lds_dwordx4 v[218:219], off
	v_lshl_add_u64 v[218:219], v[146:147], 0, s[28:29]
	s_mov_b32 m0, s57
	s_nop 0
	global_load_lds_dwordx4 v[218:219], off
	s_waitcnt vmcnt(8)
	s_waitcnt lgkmcnt(0)
	s_barrier
	s_waitcnt lgkmcnt(0)
	v_mfma_f32_16x16x32_bf16 v[14:17], v[152:155], v[184:187], v[14:17]
	v_mfma_f32_16x16x32_bf16 v[10:13], v[160:163], v[184:187], v[10:13]
	v_mfma_f32_16x16x32_bf16 v[6:9], v[152:155], v[192:195], v[6:9]
	v_mfma_f32_16x16x32_bf16 v[18:21], v[160:163], v[192:195], v[18:21]
	v_mfma_f32_16x16x32_bf16 v[22:25], v[152:155], v[202:205], v[22:25]
	v_mfma_f32_16x16x32_bf16 v[34:37], v[160:163], v[202:205], v[34:37]
	v_mfma_f32_16x16x32_bf16 v[26:29], v[152:155], v[210:213], v[26:29]
	v_mfma_f32_16x16x32_bf16 v[30:33], v[160:163], v[210:213], v[30:33]
	v_mfma_f32_16x16x32_bf16 v[14:17], v[156:159], v[188:191], v[14:17]
	v_mfma_f32_16x16x32_bf16 v[10:13], v[164:167], v[188:191], v[10:13]
	v_mfma_f32_16x16x32_bf16 v[6:9], v[156:159], v[196:199], v[6:9]
	v_mfma_f32_16x16x32_bf16 v[18:21], v[164:167], v[196:199], v[18:21]
	v_mfma_f32_16x16x32_bf16 v[22:25], v[156:159], v[206:209], v[22:25]
	v_mfma_f32_16x16x32_bf16 v[34:37], v[164:167], v[206:209], v[34:37]
	v_mfma_f32_16x16x32_bf16 v[26:29], v[156:159], v[214:217], v[26:29]
	v_mfma_f32_16x16x32_bf16 v[30:33], v[164:167], v[214:217], v[30:33]
	v_mfma_f32_16x16x32_bf16 v[66:69], v[168:171], v[184:187], v[66:69]
	v_mfma_f32_16x16x32_bf16 v[98:101], v[176:179], v[184:187], v[98:101]
	v_mfma_f32_16x16x32_bf16 v[62:65], v[168:171], v[192:195], v[62:65]
	v_mfma_f32_16x16x32_bf16 v[94:97], v[176:179], v[192:195], v[94:97]
	v_mfma_f32_16x16x32_bf16 v[58:61], v[168:171], v[202:205], v[58:61]
	v_mfma_f32_16x16x32_bf16 v[90:93], v[176:179], v[202:205], v[90:93]
	v_mfma_f32_16x16x32_bf16 v[54:57], v[168:171], v[210:213], v[54:57]
	v_mfma_f32_16x16x32_bf16 v[86:89], v[176:179], v[210:213], v[86:89]
	v_mfma_f32_16x16x32_bf16 v[66:69], v[172:175], v[188:191], v[66:69]
	v_mfma_f32_16x16x32_bf16 v[98:101], v[180:183], v[188:191], v[98:101]
	v_mfma_f32_16x16x32_bf16 v[62:65], v[172:175], v[196:199], v[62:65]
	v_mfma_f32_16x16x32_bf16 v[94:97], v[180:183], v[196:199], v[94:97]
	v_mfma_f32_16x16x32_bf16 v[58:61], v[172:175], v[206:209], v[58:61]
	v_mfma_f32_16x16x32_bf16 v[90:93], v[180:183], v[206:209], v[90:93]
	v_mfma_f32_16x16x32_bf16 v[54:57], v[172:175], v[214:217], v[54:57]
	v_mfma_f32_16x16x32_bf16 v[86:89], v[180:183], v[214:217], v[86:89]
	s_barrier
	s_mov_b32 m0, s58
	v_lshl_add_u64 v[218:219], s[24:25], 0, v[138:139]
	s_cselect_b32 s54, 0, s23
	s_cselect_b32 s55, 0, s22
	s_add_u32 s28, s24, 0x80000
	ds_read_b128 v[184:187], v150 offset:16384
	ds_read_b128 v[188:191], v150 offset:17408
	ds_read_b128 v[192:195], v150 offset:18432
	ds_read_b128 v[196:199], v150 offset:19456
	ds_read_b128 v[202:205], v150 offset:20480
	ds_read_b128 v[206:209], v150 offset:21504
	ds_read_b128 v[210:213], v150 offset:22528
	ds_read_b128 v[214:217], v150 offset:23552
	global_load_lds_dwordx4 v[218:219], off
	v_lshl_add_u64 v[220:221], s[24:25], 0, v[134:135]
	s_mov_b32 m0, s59
	s_addc_u32 s29, s25, 0
	s_add_i32 s56, s56, s38
	global_load_lds_dwordx4 v[220:221], off
	v_lshl_add_u64 v[222:223], s[28:29], 0, v[138:139]
	s_mov_b32 m0, s56
	s_nop 0
	global_load_lds_dwordx4 v[222:223], off
	v_lshl_add_u64 v[222:223], s[28:29], 0, v[134:135]
	s_add_i32 m0, s56, 0x2000
	s_and_b64 s[28:29], s[52:53], s[4:5]
	s_and_b64 s[28:29], s[28:29], exec
	s_cselect_b32 s28, s18, s16
	s_cselect_b32 s29, s19, s17
	s_add_u32 s28, s28, s55
	s_addc_u32 s29, s29, s54
	global_load_lds_dwordx4 v[222:223], off
	v_lshl_add_u64 v[222:223], s[28:29], 0, v[140:141]
	s_mov_b32 m0, s11
	v_lshl_add_u64 v[224:225], s[28:29], 0, v[136:137]
	global_load_lds_dwordx4 v[222:223], off
	s_mov_b32 m0, s40
	s_nop 0
	global_load_lds_dwordx4 v[224:225], off
	s_waitcnt vmcnt(8)
	s_waitcnt lgkmcnt(0)
	s_barrier
; #define PG8_STAGE_A(bufoff, base_, nx_, kb_, h_) do { if (GATHER) { if (nx_) PG8_STAGE_G(bufoff, kb_, goN, h_); else PG8_STAGE_G(bufoff, kb_, goC, h_); } \
;         else PG8_STAGE(bufoff, (base_) + (kb_) + (h_) * hstep, voffA); } while (0)
; #define PG8_LDA(dst, b, h) do { _Pragma("unroll") for (int m = 0; m < 4; ++m) _Pragma("unroll") for (int k = 0; k < 2; ++k) dst[m][k] = *(const LAS bf16x8*)(lds + PG8_SA(b, h) + aoff + m * 2048 + k * 1024); } while (0)
; #define PG8_LDB(dst, b, h) do { _Pragma("unroll") for (int n = 0; n < 2; ++n) _Pragma("unroll") for (int k = 0; k < 2; ++k) dst[n][k] = *(const LAS bf16x8*)(lds + PG8_SB(b, h) + boff + n * 2048 + k * 1024); } while (0)
; #define PG8_MMA(ai, bj, At, Bt) do { __builtin_amdgcn_s_setprio(1); _Pragma("unroll") for (int m = 0; m < 4; ++m) _Pragma("unroll") for (int n = 0; n < 2; ++n) _Pragma("unroll") for (int k = 0; k < 2; ++k) \
;         acc[ai][bj][m][n] = __builtin_amdgcn_mfma_f32_16x16x32_bf16(Bt[n][k], At[m][k], acc[ai][bj][m][n], 0, 0, 0); __builtin_amdgcn_s_setprio(0); } while (0)
; #define PG8_WAIT_V(n) asm volatile("s_waitcnt vmcnt(" #n ")" ::: "memory")
; #define PG8_WAIT_L(n) asm volatile("s_waitcnt lgkmcnt(" #n ")" ::: "memory")
; #define PG8_BAR __builtin_amdgcn_s_barrier()
; #define PG8_SCHED __builtin_amdgcn_sched_barrier(0)
; template <class Epi, class Sched, bool GATHER = false>
; __device__ __forceinline__ void gemm_phase(LAS unsigned char* lds, const Gemm g, const Sched& S, const Epi& E, const int tid) {
;     ...
;             PG8_WAIT_V(8); PG8_WAIT_L(0); PG8_BAR; PG8_MMA(1, 0, At, B0); PG8_MMA(1, 1, At, B1); PG8_BAR; PG8_SCHED;
;             PG8_LDB(B0, 1, 0); PG8_LDB(B1, 1, 1); PG8_SCHED; PG8_LDA(At, 1, 0); PG8_STAGE_A(PG8_SA(0, 1), (last ? nA : cA), last, kb2, 1);
;             PG8_WAIT_V(8); PG8_WAIT_L(0); PG8_BAR; PG8_MMA(0, 0, At, B0); PG8_MMA(0, 1, At, B1); PG8_BAR; PG8_SCHED;
	s_waitcnt lgkmcnt(0)
	v_mfma_f32_16x16x32_bf16 v[50:53], v[152:155], v[184:187], v[50:53]
	v_mfma_f32_16x16x32_bf16 v[82:85], v[160:163], v[184:187], v[82:85]
	v_mfma_f32_16x16x32_bf16 v[46:49], v[152:155], v[192:195], v[46:49]
	v_mfma_f32_16x16x32_bf16 v[78:81], v[160:163], v[192:195], v[78:81]
	v_mfma_f32_16x16x32_bf16 v[42:45], v[152:155], v[202:205], v[42:45]
	v_mfma_f32_16x16x32_bf16 v[74:77], v[160:163], v[202:205], v[74:77]
	v_mfma_f32_16x16x32_bf16 v[38:41], v[152:155], v[210:213], v[38:41]
	v_mfma_f32_16x16x32_bf16 v[70:73], v[160:163], v[210:213], v[70:73]
	v_mfma_f32_16x16x32_bf16 v[50:53], v[156:159], v[188:191], v[50:53]
	v_mfma_f32_16x16x32_bf16 v[82:85], v[164:167], v[188:191], v[82:85]
	v_mfma_f32_16x16x32_bf16 v[46:49], v[156:159], v[196:199], v[46:49]
	v_mfma_f32_16x16x32_bf16 v[78:81], v[164:167], v[196:199], v[78:81]
	v_mfma_f32_16x16x32_bf16 v[42:45], v[156:159], v[206:209], v[42:45]
	v_mfma_f32_16x16x32_bf16 v[74:77], v[164:167], v[206:209], v[74:77]
	v_mfma_f32_16x16x32_bf16 v[38:41], v[156:159], v[214:217], v[38:41]
	v_mfma_f32_16x16x32_bf16 v[70:73], v[164:167], v[214:217], v[70:73]
	v_mfma_f32_16x16x32_bf16 v[114:117], v[168:171], v[184:187], v[114:117]
	v_mfma_f32_16x16x32_bf16 v[130:133], v[176:179], v[184:187], v[130:133]
	v_mfma_f32_16x16x32_bf16 v[110:113], v[168:171], v[192:195], v[110:113]
	v_mfma_f32_16x16x32_bf16 v[126:129], v[176:179], v[192:195], v[126:129]
	v_mfma_f32_16x16x32_bf16 v[106:109], v[168:171], v[202:205], v[106:109]
	v_mfma_f32_16x16x32_bf16 v[122:125], v[176:179], v[202:205], v[122:125]
	v_mfma_f32_16x16x32_bf16 v[102:105], v[168:171], v[210:213], v[102:105]
	v_mfma_f32_16x16x32_bf16 v[118:121], v[176:179], v[210:213], v[118:121]
	v_mfma_f32_16x16x32_bf16 v[114:117], v[172:175], v[188:191], v[114:117]
	v_mfma_f32_16x16x32_bf16 v[130:133], v[180:183], v[188:191], v[130:133]
	v_mfma_f32_16x16x32_bf16 v[110:113], v[172:175], v[196:199], v[110:113]
	v_mfma_f32_16x16x32_bf16 v[126:129], v[180:183], v[196:199], v[126:129]
	v_mfma_f32_16x16x32_bf16 v[106:109], v[172:175], v[206:209], v[106:109]
	v_mfma_f32_16x16x32_bf16 v[122:125], v[180:183], v[206:209], v[122:125]
	v_mfma_f32_16x16x32_bf16 v[102:105], v[172:175], v[214:217], v[102:105]
	v_mfma_f32_16x16x32_bf16 v[118:121], v[180:183], v[214:217], v[118:121]
	s_barrier
	s_add_i32 s52, 0, 0x18000
	v_add_u32_e32 v2, s52, v1
	s_add_i32 s53, 0, 0x1c000
	ds_read_b128 v[152:155], v2
	ds_read_b128 v[156:159], v2 offset:1024
	ds_read_b128 v[160:163], v2 offset:2048
	ds_read_b128 v[164:167], v2 offset:3072
	v_add_u32_e32 v2, s53, v1
	ds_read_b128 v[168:171], v2
	ds_read_b128 v[172:175], v2 offset:1024
	ds_read_b128 v[176:179], v2 offset:2048
	ds_read_b128 v[180:183], v2 offset:3072
	s_add_u32 s28, s28, 0x80000
	s_addc_u32 s29, s29, 0
	s_mov_b32 m0, s41
	v_lshl_add_u64 v[226:227], s[28:29], 0, v[140:141]
	ds_read_b128 v[184:187], v150 offset:32768
	ds_read_b128 v[188:191], v150 offset:33792
	ds_read_b128 v[192:195], v150 offset:34816
	ds_read_b128 v[196:199], v150 offset:35840
	ds_read_b128 v[202:205], v150 offset:36864
	ds_read_b128 v[206:209], v150 offset:37888
	ds_read_b128 v[210:213], v150 offset:38912
	ds_read_b128 v[214:217], v150 offset:39936
	global_load_lds_dwordx4 v[226:227], off
	v_lshl_add_u64 v[226:227], s[28:29], 0, v[136:137]
	s_mov_b32 m0, s42
	s_nop 0
	global_load_lds_dwordx4 v[226:227], off
	s_waitcnt vmcnt(8)
	s_waitcnt lgkmcnt(0)
	s_barrier
	s_waitcnt lgkmcnt(0)
	v_mfma_f32_16x16x32_bf16 v[14:17], v[152:155], v[184:187], v[14:17]
	v_mfma_f32_16x16x32_bf16 v[10:13], v[160:163], v[184:187], v[10:13]
	v_mfma_f32_16x16x32_bf16 v[6:9], v[152:155], v[192:195], v[6:9]
	v_mfma_f32_16x16x32_bf16 v[18:21], v[160:163], v[192:195], v[18:21]
	v_mfma_f32_16x16x32_bf16 v[22:25], v[152:155], v[202:205], v[22:25]
	v_mfma_f32_16x16x32_bf16 v[34:37], v[160:163], v[202:205], v[34:37]
	v_mfma_f32_16x16x32_bf16 v[26:29], v[152:155], v[210:213], v[26:29]
	v_mfma_f32_16x16x32_bf16 v[30:33], v[160:163], v[210:213], v[30:33]
	v_mfma_f32_16x16x32_bf16 v[14:17], v[156:159], v[188:191], v[14:17]
	v_mfma_f32_16x16x32_bf16 v[10:13], v[164:167], v[188:191], v[10:13]
	v_mfma_f32_16x16x32_bf16 v[6:9], v[156:159], v[196:199], v[6:9]
	v_mfma_f32_16x16x32_bf16 v[18:21], v[164:167], v[196:199], v[18:21]
	v_mfma_f32_16x16x32_bf16 v[22:25], v[156:159], v[206:209], v[22:25]
	v_mfma_f32_16x16x32_bf16 v[34:37], v[164:167], v[206:209], v[34:37]
	v_mfma_f32_16x16x32_bf16 v[26:29], v[156:159], v[214:217], v[26:29]
	v_mfma_f32_16x16x32_bf16 v[30:33], v[164:167], v[214:217], v[30:33]
	v_mfma_f32_16x16x32_bf16 v[66:69], v[168:171], v[184:187], v[66:69]
	v_mfma_f32_16x16x32_bf16 v[98:101], v[176:179], v[184:187], v[98:101]
	v_mfma_f32_16x16x32_bf16 v[62:65], v[168:171], v[192:195], v[62:65]
	v_mfma_f32_16x16x32_bf16 v[94:97], v[176:179], v[192:195], v[94:97]
	v_mfma_f32_16x16x32_bf16 v[58:61], v[168:171], v[202:205], v[58:61]
	v_mfma_f32_16x16x32_bf16 v[90:93], v[176:179], v[202:205], v[90:93]
	v_mfma_f32_16x16x32_bf16 v[54:57], v[168:171], v[210:213], v[54:57]
	v_mfma_f32_16x16x32_bf16 v[86:89], v[176:179], v[210:213], v[86:89]
	v_mfma_f32_16x16x32_bf16 v[66:69], v[172:175], v[188:191], v[66:69]
	v_mfma_f32_16x16x32_bf16 v[98:101], v[180:183], v[188:191], v[98:101]
	v_mfma_f32_16x16x32_bf16 v[62:65], v[172:175], v[196:199], v[62:65]
	v_mfma_f32_16x16x32_bf16 v[94:97], v[180:183], v[196:199], v[94:97]
	v_mfma_f32_16x16x32_bf16 v[58:61], v[172:175], v[206:209], v[58:61]
	v_mfma_f32_16x16x32_bf16 v[90:93], v[180:183], v[206:209], v[90:93]
	v_mfma_f32_16x16x32_bf16 v[54:57], v[172:175], v[214:217], v[54:57]
	v_mfma_f32_16x16x32_bf16 v[86:89], v[180:183], v[214:217], v[86:89]
	s_barrier
; #define PG8_STAGE_A(bufoff, base_, nx_, kb_, h_) do { if (GATHER) { if (nx_) PG8_STAGE_G(bufoff, kb_, goN, h_); else PG8_STAGE_G(bufoff, kb_, goC, h_); } \
;         else PG8_STAGE(bufoff, (base_) + (kb_) + (h_) * hstep, voffA); } while (0)
; #define PG8_STAGE(bufoff, gbase, voff) do { _Pragma("unroll") for (int _i = 0; _i < 2; ++_i) \
;         __builtin_amdgcn_global_load_lds((const unsigned*)((const char*)(gbase) + (voff)[_i]), (LAS unsigned*)(lds + (bufoff) + ldsw + _i * 8192), 16, 0, 0); } while (0)
; #define PG8_LDA(dst, b, h) do { _Pragma("unroll") for (int m = 0; m < 4; ++m) _Pragma("unroll") for (int k = 0; k < 2; ++k) dst[m][k] = *(const LAS bf16x8*)(lds + PG8_SA(b, h) + aoff + m * 2048 + k * 1024); } while (0)
; #define PG8_MMA(ai, bj, At, Bt) do { __builtin_amdgcn_s_setprio(1); _Pragma("unroll") for (int m = 0; m < 4; ++m) _Pragma("unroll") for (int n = 0; n < 2; ++n) _Pragma("unroll") for (int k = 0; k < 2; ++k) \
;         acc[ai][bj][m][n] = __builtin_amdgcn_mfma_f32_16x16x32_bf16(Bt[n][k], At[m][k], acc[ai][bj][m][n], 0, 0, 0); __builtin_amdgcn_s_setprio(0); } while (0)
; #define PG8_WAIT_V(n) asm volatile("s_waitcnt vmcnt(" #n ")" ::: "memory")
; #define PG8_WAIT_L(n) asm volatile("s_waitcnt lgkmcnt(" #n ")" ::: "memory")
; #define PG8_BAR __builtin_amdgcn_s_barrier()
; #define PG8_SCHED __builtin_amdgcn_sched_barrier(0)
; template <class Epi, class Sched, bool GATHER = false>
; __device__ __forceinline__ void gemm_phase(LAS unsigned char* lds, const Gemm g, const Sched& S, const Epi& E, const int tid) {
;     ...
;         for (int t = 0; t < nt; t += 2) {
;             const bool last = (t == nt - 2);
;             const char* a1 = cA + (size_t)(t + 1) * kstep;
;             const char* a2 = last ? nA : cA + (size_t)(t + 2) * kstep; const char* b2 = last ? nB : cB + (size_t)(t + 2) * kstep;
;             const char* a3 = a2 + kstep; const char* b3 = b2 + kstep;
;     ...
;             PG8_LDA(At, 1, 1); PG8_STAGE(PG8_SB(1, 0), b3, voffB); PG8_STAGE(PG8_SB(1, 1), b3 + hstep, voffB); PG8_STAGE_A(PG8_SA(1, 0), (last ? nA : cA), last, kb3, 0);
;             PG8_WAIT_V(8); PG8_WAIT_L(0); PG8_BAR; PG8_MMA(1, 0, At, B0); PG8_MMA(1, 1, At, B1); PG8_BAR; PG8_SCHED;
	s_add_i32 s28, s52, s38
	v_lshl_add_u64 v[218:219], v[218:219], 0, s[0:1]
	s_mov_b32 m0, s28
	ds_read_b128 v[184:187], v150 offset:49152
	ds_read_b128 v[188:191], v150 offset:50176
	ds_read_b128 v[192:195], v150 offset:51200
	ds_read_b128 v[196:199], v150 offset:52224
	ds_read_b128 v[202:205], v150 offset:53248
	ds_read_b128 v[206:209], v150 offset:54272
	ds_read_b128 v[210:213], v150 offset:55296
	ds_read_b128 v[214:217], v150 offset:56320
	global_load_lds_dwordx4 v[218:219], off
	s_add_i32 m0, s28, 0x2000
	s_add_u32 s24, s24, 0x80080
	v_lshl_add_u64 v[218:219], v[220:221], 0, s[0:1]
	s_addc_u32 s25, s25, 0
	s_add_i32 s28, s53, s38
	global_load_lds_dwordx4 v[218:219], off
	v_lshl_add_u64 v[218:219], s[24:25], 0, v[138:139]
	s_mov_b32 m0, s28
	s_nop 0
	global_load_lds_dwordx4 v[218:219], off
	v_lshl_add_u64 v[218:219], s[24:25], 0, v[134:135]
	s_add_i32 m0, s28, 0x2000
	s_nop 0
	global_load_lds_dwordx4 v[218:219], off
	v_lshl_add_u64 v[218:219], v[222:223], 0, s[0:1]
	s_mov_b32 m0, s44
	s_nop 0
	global_load_lds_dwordx4 v[218:219], off
	v_lshl_add_u64 v[218:219], v[224:225], 0, s[0:1]
	s_mov_b32 m0, s45
	s_nop 0
	global_load_lds_dwordx4 v[218:219], off
	s_waitcnt vmcnt(8)
	s_waitcnt lgkmcnt(0)
	s_barrier
	s_waitcnt lgkmcnt(0)
	v_mfma_f32_16x16x32_bf16 v[50:53], v[152:155], v[184:187], v[50:53]
	v_mfma_f32_16x16x32_bf16 v[82:85], v[160:163], v[184:187], v[82:85]
	v_mfma_f32_16x16x32_bf16 v[46:49], v[152:155], v[192:195], v[46:49]
	v_mfma_f32_16x16x32_bf16 v[78:81], v[160:163], v[192:195], v[78:81]
	v_mfma_f32_16x16x32_bf16 v[42:45], v[152:155], v[202:205], v[42:45]
	v_mfma_f32_16x16x32_bf16 v[74:77], v[160:163], v[202:205], v[74:77]
	v_mfma_f32_16x16x32_bf16 v[38:41], v[152:155], v[210:213], v[38:41]
	v_mfma_f32_16x16x32_bf16 v[70:73], v[160:163], v[210:213], v[70:73]
	v_mfma_f32_16x16x32_bf16 v[50:53], v[156:159], v[188:191], v[50:53]
	v_mfma_f32_16x16x32_bf16 v[82:85], v[164:167], v[188:191], v[82:85]
	v_mfma_f32_16x16x32_bf16 v[46:49], v[156:159], v[196:199], v[46:49]
	v_mfma_f32_16x16x32_bf16 v[78:81], v[164:167], v[196:199], v[78:81]
	v_mfma_f32_16x16x32_bf16 v[42:45], v[156:159], v[206:209], v[42:45]
	v_mfma_f32_16x16x32_bf16 v[74:77], v[164:167], v[206:209], v[74:77]
	v_mfma_f32_16x16x32_bf16 v[38:41], v[156:159], v[214:217], v[38:41]
	v_mfma_f32_16x16x32_bf16 v[70:73], v[164:167], v[214:217], v[70:73]
	v_mfma_f32_16x16x32_bf16 v[114:117], v[168:171], v[184:187], v[114:117]
	v_mfma_f32_16x16x32_bf16 v[130:133], v[176:179], v[184:187], v[130:133]
	v_mfma_f32_16x16x32_bf16 v[110:113], v[168:171], v[192:195], v[110:113]
	v_mfma_f32_16x16x32_bf16 v[126:129], v[176:179], v[192:195], v[126:129]
	v_mfma_f32_16x16x32_bf16 v[106:109], v[168:171], v[202:205], v[106:109]
	v_mfma_f32_16x16x32_bf16 v[122:125], v[176:179], v[202:205], v[122:125]
	v_mfma_f32_16x16x32_bf16 v[102:105], v[168:171], v[210:213], v[102:105]
	v_mfma_f32_16x16x32_bf16 v[118:121], v[176:179], v[210:213], v[118:121]
	v_mfma_f32_16x16x32_bf16 v[114:117], v[172:175], v[188:191], v[114:117]
	v_mfma_f32_16x16x32_bf16 v[130:133], v[180:183], v[188:191], v[130:133]
	v_mfma_f32_16x16x32_bf16 v[110:113], v[172:175], v[196:199], v[110:113]
	v_mfma_f32_16x16x32_bf16 v[126:129], v[180:183], v[196:199], v[126:129]
	v_mfma_f32_16x16x32_bf16 v[106:109], v[172:175], v[206:209], v[106:109]
	v_mfma_f32_16x16x32_bf16 v[122:125], v[180:183], v[206:209], v[122:125]
	v_mfma_f32_16x16x32_bf16 v[102:105], v[172:175], v[214:217], v[102:105]
	v_mfma_f32_16x16x32_bf16 v[118:121], v[180:183], v[214:217], v[118:121]
	s_barrier
	s_add_i32 s51, s51, 2
	s_cmp_gt_u32 s51, 29
	s_mov_b64 s[28:29], s[22:23]
	s_cbranch_scc0 .LBB0_247
	s_and_b64 vcc, exec, s[8:9]
	s_cbranch_vccz .LBB0_250
	s_barrier

; #define PG8_STAGE_A(bufoff, base_, nx_, kb_, h_) do { if (GATHER) { if (nx_) PG8_STAGE_G(bufoff, kb_, goN, h_); else PG8_STAGE_G(bufoff, kb_, goC, h_); } \
;         else PG8_STAGE(bufoff, (base_) + (kb_) + (h_) * hstep, voffA); } while (0)
; #define PG8_STAGE(bufoff, gbase, voff) do { _Pragma("unroll") for (int _i = 0; _i < 2; ++_i) \
;         __builtin_amdgcn_global_load_lds((const unsigned*)((const char*)(gbase) + (voff)[_i]), (LAS unsigned*)(lds + (bufoff) + ldsw + _i * 8192), 16, 0, 0); } while (0)
; #define PG8_LDA(dst, b, h) do { _Pragma("unroll") for (int m = 0; m < 4; ++m) _Pragma("unroll") for (int k = 0; k < 2; ++k) dst[m][k] = *(const LAS bf16x8*)(lds + PG8_SA(b, h) + aoff + m * 2048 + k * 1024); } while (0)
; #define PG8_LDB(dst, b, h) do { _Pragma("unroll") for (int n = 0; n < 2; ++n) _Pragma("unroll") for (int k = 0; k < 2; ++k) dst[n][k] = *(const LAS bf16x8*)(lds + PG8_SB(b, h) + boff + n * 2048 + k * 1024); } while (0)
; #define PG8_MMA(ai, bj, At, Bt) do { __builtin_amdgcn_s_setprio(1); _Pragma("unroll") for (int m = 0; m < 4; ++m) _Pragma("unroll") for (int n = 0; n < 2; ++n) _Pragma("unroll") for (int k = 0; k < 2; ++k) \
;         acc[ai][bj][m][n] = __builtin_amdgcn_mfma_f32_16x16x32_bf16(Bt[n][k], At[m][k], acc[ai][bj][m][n], 0, 0, 0); __builtin_amdgcn_s_setprio(0); } while (0)
; #define PG8_WAIT_V(n) asm volatile("s_waitcnt vmcnt(" #n ")" ::: "memory")
; #define PG8_WAIT_L(n) asm volatile("s_waitcnt lgkmcnt(" #n ")" ::: "memory")
; #define PG8_BAR __builtin_amdgcn_s_barrier()
; #define PG8_SCHED __builtin_amdgcn_sched_barrier(0)
; template <class Epi, class Sched, bool GATHER = false>
; __device__ __forceinline__ void gemm_phase(LAS unsigned char* lds, const Gemm g, const Sched& S, const Epi& E, const int tid) {
;     ...
;             PG8_LDB(B0, 0, 0); PG8_LDB(B1, 0, 1); PG8_SCHED; PG8_LDA(At, 0, 0); PG8_STAGE_A(PG8_SA(1, 1), cA, false, kb1, 1);
;             PG8_WAIT_V(8); PG8_WAIT_L(0); PG8_BAR; PG8_MMA(0, 0, At, B0); PG8_MMA(0, 1, At, B1); PG8_BAR; PG8_SCHED;
;             PG8_LDA(At, 0, 1); PG8_STAGE(PG8_SB(0, 0), b2, voffB); PG8_STAGE(PG8_SB(0, 1), b2 + hstep, voffB); PG8_STAGE_A(PG8_SA(0, 0), (last ? nA : cA), last, kb2, 0);
;             PG8_WAIT_V(8); PG8_WAIT_L(0); PG8_BAR; PG8_MMA(1, 0, At, B0); PG8_MMA(1, 1, At, B1); PG8_BAR; PG8_SCHED;
.LBB0_1128:
	s_add_u32 s22, s28, 0x100
	s_addc_u32 s23, s29, 0
	s_add_u32 s52, s47, s28
	s_addc_u32 s53, s48, s29
	s_add_i32 s24, 0, 0x10000
	s_add_i32 s54, 0, 0x14000
	v_add_u32_e32 v2, s24, v148
	ds_read_b128 v[152:155], v2
	ds_read_b128 v[156:159], v2 offset:1024
	ds_read_b128 v[160:163], v2 offset:2048
	ds_read_b128 v[164:167], v2 offset:3072
	v_add_u32_e32 v2, s54, v148
	ds_read_b128 v[168:171], v2
	ds_read_b128 v[172:175], v2 offset:1024
	ds_read_b128 v[176:179], v2 offset:2048
	ds_read_b128 v[180:183], v2 offset:3072
	s_add_i32 s56, s24, s33
	s_add_i32 m0, s9, 0xc000
	s_add_i32 s55, s9, 0xe000
	s_add_i32 s57, s56, 0x2000
	s_cmp_eq_u32 s49, 28
	s_cselect_b64 s[50:51], -1, 0
	s_and_b64 s[24:25], s[50:51], exec
	s_cselect_b32 s25, s15, s53
	s_cselect_b32 s24, s17, s52
	v_lshl_add_u64 v[218:219], v[4:5], 0, s[28:29]
	ds_read_b128 v[184:187], v150
	ds_read_b128 v[188:191], v150 offset:1024
	ds_read_b128 v[192:195], v150 offset:2048
	ds_read_b128 v[196:199], v150 offset:3072
	ds_read_b128 v[202:205], v150 offset:4096
	ds_read_b128 v[206:209], v150 offset:5120
	ds_read_b128 v[210:213], v150 offset:6144
	ds_read_b128 v[214:217], v150 offset:7168
	global_load_lds_dwordx4 v[218:219], off
	v_lshl_add_u64 v[218:219], v[146:147], 0, s[28:29]
	s_mov_b32 m0, s55
	s_nop 0
	global_load_lds_dwordx4 v[218:219], off
	s_waitcnt vmcnt(8)
	s_waitcnt lgkmcnt(0)
	s_barrier
	s_waitcnt lgkmcnt(0)
	v_mfma_f32_16x16x32_bf16 v[86:89], v[152:155], v[184:187], v[86:89]
	v_mfma_f32_16x16x32_bf16 v[18:21], v[160:163], v[184:187], v[18:21]
	v_mfma_f32_16x16x32_bf16 v[6:9], v[152:155], v[192:195], v[6:9]
	v_mfma_f32_16x16x32_bf16 v[22:25], v[160:163], v[192:195], v[22:25]
	v_mfma_f32_16x16x32_bf16 v[10:13], v[152:155], v[202:205], v[10:13]
	v_mfma_f32_16x16x32_bf16 v[26:29], v[160:163], v[202:205], v[26:29]
	v_mfma_f32_16x16x32_bf16 v[14:17], v[152:155], v[210:213], v[14:17]
	v_mfma_f32_16x16x32_bf16 v[30:33], v[160:163], v[210:213], v[30:33]
	v_mfma_f32_16x16x32_bf16 v[86:89], v[156:159], v[188:191], v[86:89]
	v_mfma_f32_16x16x32_bf16 v[18:21], v[164:167], v[188:191], v[18:21]
	v_mfma_f32_16x16x32_bf16 v[6:9], v[156:159], v[196:199], v[6:9]
	v_mfma_f32_16x16x32_bf16 v[22:25], v[164:167], v[196:199], v[22:25]
	v_mfma_f32_16x16x32_bf16 v[10:13], v[156:159], v[206:209], v[10:13]
	v_mfma_f32_16x16x32_bf16 v[26:29], v[164:167], v[206:209], v[26:29]
	v_mfma_f32_16x16x32_bf16 v[14:17], v[156:159], v[214:217], v[14:17]
	v_mfma_f32_16x16x32_bf16 v[30:33], v[164:167], v[214:217], v[30:33]
	v_mfma_f32_16x16x32_bf16 v[34:37], v[168:171], v[184:187], v[34:37]
	v_mfma_f32_16x16x32_bf16 v[50:53], v[176:179], v[184:187], v[50:53]
	v_mfma_f32_16x16x32_bf16 v[38:41], v[168:171], v[192:195], v[38:41]
	v_mfma_f32_16x16x32_bf16 v[58:61], v[176:179], v[192:195], v[58:61]
	v_mfma_f32_16x16x32_bf16 v[42:45], v[168:171], v[202:205], v[42:45]
	v_mfma_f32_16x16x32_bf16 v[66:69], v[176:179], v[202:205], v[66:69]
	v_mfma_f32_16x16x32_bf16 v[46:49], v[168:171], v[210:213], v[46:49]
	v_mfma_f32_16x16x32_bf16 v[74:77], v[176:179], v[210:213], v[74:77]
	v_mfma_f32_16x16x32_bf16 v[34:37], v[172:175], v[188:191], v[34:37]
	v_mfma_f32_16x16x32_bf16 v[50:53], v[180:183], v[188:191], v[50:53]
	v_mfma_f32_16x16x32_bf16 v[38:41], v[172:175], v[196:199], v[38:41]
	v_mfma_f32_16x16x32_bf16 v[58:61], v[180:183], v[196:199], v[58:61]
	v_mfma_f32_16x16x32_bf16 v[42:45], v[172:175], v[206:209], v[42:45]
	v_mfma_f32_16x16x32_bf16 v[66:69], v[180:183], v[206:209], v[66:69]
	v_mfma_f32_16x16x32_bf16 v[46:49], v[172:175], v[214:217], v[46:49]
	v_mfma_f32_16x16x32_bf16 v[74:77], v[180:183], v[214:217], v[74:77]
	s_barrier
	s_mov_b32 m0, s56
	v_lshl_add_u64 v[218:219], s[24:25], 0, v[136:137]
	s_cselect_b32 s52, 0, s23
	s_cselect_b32 s53, 0, s22
	s_add_u32 s28, s24, 0x80000
	ds_read_b128 v[184:187], v150 offset:16384
	ds_read_b128 v[188:191], v150 offset:17408
	ds_read_b128 v[192:195], v150 offset:18432
	ds_read_b128 v[196:199], v150 offset:19456
	ds_read_b128 v[202:205], v150 offset:20480
	ds_read_b128 v[206:209], v150 offset:21504
	ds_read_b128 v[210:213], v150 offset:22528
	ds_read_b128 v[214:217], v150 offset:23552
	global_load_lds_dwordx4 v[218:219], off
	v_lshl_add_u64 v[220:221], s[24:25], 0, v[140:141]
	s_mov_b32 m0, s57
	s_addc_u32 s29, s25, 0
	s_add_i32 s54, s54, s33
	global_load_lds_dwordx4 v[220:221], off
	v_lshl_add_u64 v[222:223], s[28:29], 0, v[136:137]
	s_mov_b32 m0, s54
	s_nop 0
	global_load_lds_dwordx4 v[222:223], off
	v_lshl_add_u64 v[222:223], s[28:29], 0, v[140:141]
	s_add_i32 m0, s54, 0x2000
	s_and_b64 s[28:29], s[50:51], s[4:5]
	s_and_b64 s[28:29], s[28:29], exec
	s_cselect_b32 s28, s18, s10
	s_cselect_b32 s29, s19, s11
	s_add_u32 s28, s28, s53
	s_addc_u32 s29, s29, s52
	global_load_lds_dwordx4 v[222:223], off
	v_lshl_add_u64 v[222:223], s[28:29], 0, v[134:135]
	s_mov_b32 m0, s9
	v_lshl_add_u64 v[224:225], s[28:29], 0, v[138:139]
	global_load_lds_dwordx4 v[222:223], off
	s_mov_b32 m0, s38
	s_nop 0
	global_load_lds_dwordx4 v[224:225], off
	s_waitcnt vmcnt(8)
	s_waitcnt lgkmcnt(0)
	s_barrier
; #define PG8_STAGE_A(bufoff, base_, nx_, kb_, h_) do { if (GATHER) { if (nx_) PG8_STAGE_G(bufoff, kb_, goN, h_); else PG8_STAGE_G(bufoff, kb_, goC, h_); } \
;         else PG8_STAGE(bufoff, (base_) + (kb_) + (h_) * hstep, voffA); } while (0)
; #define PG8_LDA(dst, b, h) do { _Pragma("unroll") for (int m = 0; m < 4; ++m) _Pragma("unroll") for (int k = 0; k < 2; ++k) dst[m][k] = *(const LAS bf16x8*)(lds + PG8_SA(b, h) + aoff + m * 2048 + k * 1024); } while (0)
; #define PG8_LDB(dst, b, h) do { _Pragma("unroll") for (int n = 0; n < 2; ++n) _Pragma("unroll") for (int k = 0; k < 2; ++k) dst[n][k] = *(const LAS bf16x8*)(lds + PG8_SB(b, h) + boff + n * 2048 + k * 1024); } while (0)
; #define PG8_MMA(ai, bj, At, Bt) do { __builtin_amdgcn_s_setprio(1); _Pragma("unroll") for (int m = 0; m < 4; ++m) _Pragma("unroll") for (int n = 0; n < 2; ++n) _Pragma("unroll") for (int k = 0; k < 2; ++k) \
;         acc[ai][bj][m][n] = __builtin_amdgcn_mfma_f32_16x16x32_bf16(Bt[n][k], At[m][k], acc[ai][bj][m][n], 0, 0, 0); __builtin_amdgcn_s_setprio(0); } while (0)
; #define PG8_WAIT_V(n) asm volatile("s_waitcnt vmcnt(" #n ")" ::: "memory")
; #define PG8_WAIT_L(n) asm volatile("s_waitcnt lgkmcnt(" #n ")" ::: "memory")
; #define PG8_BAR __builtin_amdgcn_s_barrier()
; #define PG8_SCHED __builtin_amdgcn_sched_barrier(0)
; template <class Epi, class Sched, bool GATHER = false>
; __device__ __forceinline__ void gemm_phase(LAS unsigned char* lds, const Gemm g, const Sched& S, const Epi& E, const int tid) {
;     ...
;             PG8_WAIT_V(8); PG8_WAIT_L(0); PG8_BAR; PG8_MMA(1, 0, At, B0); PG8_MMA(1, 1, At, B1); PG8_BAR; PG8_SCHED;
;             PG8_LDB(B0, 1, 0); PG8_LDB(B1, 1, 1); PG8_SCHED; PG8_LDA(At, 1, 0); PG8_STAGE_A(PG8_SA(0, 1), (last ? nA : cA), last, kb2, 1);
;             PG8_WAIT_V(8); PG8_WAIT_L(0); PG8_BAR; PG8_MMA(0, 0, At, B0); PG8_MMA(0, 1, At, B1); PG8_BAR; PG8_SCHED;
	s_waitcnt lgkmcnt(0)
	v_mfma_f32_16x16x32_bf16 v[54:57], v[152:155], v[184:187], v[54:57]
	v_mfma_f32_16x16x32_bf16 v[78:81], v[160:163], v[184:187], v[78:81]
	v_mfma_f32_16x16x32_bf16 v[62:65], v[152:155], v[192:195], v[62:65]
	v_mfma_f32_16x16x32_bf16 v[82:85], v[160:163], v[192:195], v[82:85]
	v_mfma_f32_16x16x32_bf16 v[70:73], v[152:155], v[202:205], v[70:73]
	v_mfma_f32_16x16x32_bf16 v[98:101], v[160:163], v[202:205], v[98:101]
	v_mfma_f32_16x16x32_bf16 v[90:93], v[152:155], v[210:213], v[90:93]
	v_mfma_f32_16x16x32_bf16 v[94:97], v[160:163], v[210:213], v[94:97]
	v_mfma_f32_16x16x32_bf16 v[54:57], v[156:159], v[188:191], v[54:57]
	v_mfma_f32_16x16x32_bf16 v[78:81], v[164:167], v[188:191], v[78:81]
	v_mfma_f32_16x16x32_bf16 v[62:65], v[156:159], v[196:199], v[62:65]
	v_mfma_f32_16x16x32_bf16 v[82:85], v[164:167], v[196:199], v[82:85]
	v_mfma_f32_16x16x32_bf16 v[70:73], v[156:159], v[206:209], v[70:73]
	v_mfma_f32_16x16x32_bf16 v[98:101], v[164:167], v[206:209], v[98:101]
	v_mfma_f32_16x16x32_bf16 v[90:93], v[156:159], v[214:217], v[90:93]
	v_mfma_f32_16x16x32_bf16 v[94:97], v[164:167], v[214:217], v[94:97]
	v_mfma_f32_16x16x32_bf16 v[114:117], v[168:171], v[184:187], v[114:117]
	v_mfma_f32_16x16x32_bf16 v[130:133], v[176:179], v[184:187], v[130:133]
	v_mfma_f32_16x16x32_bf16 v[110:113], v[168:171], v[192:195], v[110:113]
	v_mfma_f32_16x16x32_bf16 v[126:129], v[176:179], v[192:195], v[126:129]
	v_mfma_f32_16x16x32_bf16 v[106:109], v[168:171], v[202:205], v[106:109]
	v_mfma_f32_16x16x32_bf16 v[122:125], v[176:179], v[202:205], v[122:125]
	v_mfma_f32_16x16x32_bf16 v[102:105], v[168:171], v[210:213], v[102:105]
	v_mfma_f32_16x16x32_bf16 v[118:121], v[176:179], v[210:213], v[118:121]
	v_mfma_f32_16x16x32_bf16 v[114:117], v[172:175], v[188:191], v[114:117]
	v_mfma_f32_16x16x32_bf16 v[130:133], v[180:183], v[188:191], v[130:133]
	v_mfma_f32_16x16x32_bf16 v[110:113], v[172:175], v[196:199], v[110:113]
	v_mfma_f32_16x16x32_bf16 v[126:129], v[180:183], v[196:199], v[126:129]
	v_mfma_f32_16x16x32_bf16 v[106:109], v[172:175], v[206:209], v[106:109]
	v_mfma_f32_16x16x32_bf16 v[122:125], v[180:183], v[206:209], v[122:125]
	v_mfma_f32_16x16x32_bf16 v[102:105], v[172:175], v[214:217], v[102:105]
	v_mfma_f32_16x16x32_bf16 v[118:121], v[180:183], v[214:217], v[118:121]
	s_barrier
	s_add_i32 s50, 0, 0x18000
	v_add_u32_e32 v2, s50, v148
	s_add_i32 s51, 0, 0x1c000
	ds_read_b128 v[152:155], v2
	ds_read_b128 v[156:159], v2 offset:1024
	ds_read_b128 v[160:163], v2 offset:2048
	ds_read_b128 v[164:167], v2 offset:3072
	v_add_u32_e32 v2, s51, v148
	ds_read_b128 v[168:171], v2
	ds_read_b128 v[172:175], v2 offset:1024
	ds_read_b128 v[176:179], v2 offset:2048
	ds_read_b128 v[180:183], v2 offset:3072
	s_add_u32 s28, s28, 0x80000
	s_addc_u32 s29, s29, 0
	s_mov_b32 m0, s39
	v_lshl_add_u64 v[226:227], s[28:29], 0, v[134:135]
	ds_read_b128 v[184:187], v150 offset:32768
	ds_read_b128 v[188:191], v150 offset:33792
	ds_read_b128 v[192:195], v150 offset:34816
	ds_read_b128 v[196:199], v150 offset:35840
	ds_read_b128 v[202:205], v150 offset:36864
	ds_read_b128 v[206:209], v150 offset:37888
	ds_read_b128 v[210:213], v150 offset:38912
	ds_read_b128 v[214:217], v150 offset:39936
	global_load_lds_dwordx4 v[226:227], off
	v_lshl_add_u64 v[226:227], s[28:29], 0, v[138:139]
	s_mov_b32 m0, s40
	s_nop 0
	global_load_lds_dwordx4 v[226:227], off
	s_waitcnt vmcnt(8)
	s_waitcnt lgkmcnt(0)
	s_barrier
	s_waitcnt lgkmcnt(0)
	v_mfma_f32_16x16x32_bf16 v[86:89], v[152:155], v[184:187], v[86:89]
	v_mfma_f32_16x16x32_bf16 v[18:21], v[160:163], v[184:187], v[18:21]
	v_mfma_f32_16x16x32_bf16 v[6:9], v[152:155], v[192:195], v[6:9]
	v_mfma_f32_16x16x32_bf16 v[22:25], v[160:163], v[192:195], v[22:25]
	v_mfma_f32_16x16x32_bf16 v[10:13], v[152:155], v[202:205], v[10:13]
	v_mfma_f32_16x16x32_bf16 v[26:29], v[160:163], v[202:205], v[26:29]
	v_mfma_f32_16x16x32_bf16 v[14:17], v[152:155], v[210:213], v[14:17]
	v_mfma_f32_16x16x32_bf16 v[30:33], v[160:163], v[210:213], v[30:33]
	v_mfma_f32_16x16x32_bf16 v[86:89], v[156:159], v[188:191], v[86:89]
	v_mfma_f32_16x16x32_bf16 v[18:21], v[164:167], v[188:191], v[18:21]
	v_mfma_f32_16x16x32_bf16 v[6:9], v[156:159], v[196:199], v[6:9]
	v_mfma_f32_16x16x32_bf16 v[22:25], v[164:167], v[196:199], v[22:25]
	v_mfma_f32_16x16x32_bf16 v[10:13], v[156:159], v[206:209], v[10:13]
	v_mfma_f32_16x16x32_bf16 v[26:29], v[164:167], v[206:209], v[26:29]
	v_mfma_f32_16x16x32_bf16 v[14:17], v[156:159], v[214:217], v[14:17]
	v_mfma_f32_16x16x32_bf16 v[30:33], v[164:167], v[214:217], v[30:33]
	v_mfma_f32_16x16x32_bf16 v[34:37], v[168:171], v[184:187], v[34:37]
	v_mfma_f32_16x16x32_bf16 v[50:53], v[176:179], v[184:187], v[50:53]
	v_mfma_f32_16x16x32_bf16 v[38:41], v[168:171], v[192:195], v[38:41]
	v_mfma_f32_16x16x32_bf16 v[58:61], v[176:179], v[192:195], v[58:61]
	v_mfma_f32_16x16x32_bf16 v[42:45], v[168:171], v[202:205], v[42:45]
	v_mfma_f32_16x16x32_bf16 v[66:69], v[176:179], v[202:205], v[66:69]
	v_mfma_f32_16x16x32_bf16 v[46:49], v[168:171], v[210:213], v[46:49]
	v_mfma_f32_16x16x32_bf16 v[74:77], v[176:179], v[210:213], v[74:77]
	v_mfma_f32_16x16x32_bf16 v[34:37], v[172:175], v[188:191], v[34:37]
	v_mfma_f32_16x16x32_bf16 v[50:53], v[180:183], v[188:191], v[50:53]
	v_mfma_f32_16x16x32_bf16 v[38:41], v[172:175], v[196:199], v[38:41]
	v_mfma_f32_16x16x32_bf16 v[58:61], v[180:183], v[196:199], v[58:61]
	v_mfma_f32_16x16x32_bf16 v[42:45], v[172:175], v[206:209], v[42:45]
	v_mfma_f32_16x16x32_bf16 v[66:69], v[180:183], v[206:209], v[66:69]
	v_mfma_f32_16x16x32_bf16 v[46:49], v[172:175], v[214:217], v[46:49]
	v_mfma_f32_16x16x32_bf16 v[74:77], v[180:183], v[214:217], v[74:77]
	s_barrier
; #define PG8_STAGE_A(bufoff, base_, nx_, kb_, h_) do { if (GATHER) { if (nx_) PG8_STAGE_G(bufoff, kb_, goN, h_); else PG8_STAGE_G(bufoff, kb_, goC, h_); } \
;         else PG8_STAGE(bufoff, (base_) + (kb_) + (h_) * hstep, voffA); } while (0)
; #define PG8_STAGE(bufoff, gbase, voff) do { _Pragma("unroll") for (int _i = 0; _i < 2; ++_i) \
;         __builtin_amdgcn_global_load_lds((const unsigned*)((const char*)(gbase) + (voff)[_i]), (LAS unsigned*)(lds + (bufoff) + ldsw + _i * 8192), 16, 0, 0); } while (0)
; #define PG8_LDA(dst, b, h) do { _Pragma("unroll") for (int m = 0; m < 4; ++m) _Pragma("unroll") for (int k = 0; k < 2; ++k) dst[m][k] = *(const LAS bf16x8*)(lds + PG8_SA(b, h) + aoff + m * 2048 + k * 1024); } while (0)
; #define PG8_MMA(ai, bj, At, Bt) do { __builtin_amdgcn_s_setprio(1); _Pragma("unroll") for (int m = 0; m < 4; ++m) _Pragma("unroll") for (int n = 0; n < 2; ++n) _Pragma("unroll") for (int k = 0; k < 2; ++k) \
;         acc[ai][bj][m][n] = __builtin_amdgcn_mfma_f32_16x16x32_bf16(Bt[n][k], At[m][k], acc[ai][bj][m][n], 0, 0, 0); __builtin_amdgcn_s_setprio(0); } while (0)
; #define PG8_WAIT_V(n) asm volatile("s_waitcnt vmcnt(" #n ")" ::: "memory")
; #define PG8_WAIT_L(n) asm volatile("s_waitcnt lgkmcnt(" #n ")" ::: "memory")
; #define PG8_BAR __builtin_amdgcn_s_barrier()
; #define PG8_SCHED __builtin_amdgcn_sched_barrier(0)
; template <class Epi, class Sched, bool GATHER = false>
; __device__ __forceinline__ void gemm_phase(LAS unsigned char* lds, const Gemm g, const Sched& S, const Epi& E, const int tid) {
;     ...
;             PG8_LDA(At, 1, 1); PG8_STAGE(PG8_SB(1, 0), b3, voffB); PG8_STAGE(PG8_SB(1, 1), b3 + hstep, voffB); PG8_STAGE_A(PG8_SA(1, 0), (last ? nA : cA), last, kb3, 0);
;             PG8_WAIT_V(8); PG8_WAIT_L(0); PG8_BAR; PG8_MMA(1, 0, At, B0); PG8_MMA(1, 1, At, B1); PG8_BAR; PG8_SCHED;
	s_add_i32 s28, s50, s33
	v_lshl_add_u64 v[218:219], v[218:219], 0, s[0:1]
	s_mov_b32 m0, s28
	ds_read_b128 v[184:187], v150 offset:49152
	ds_read_b128 v[188:191], v150 offset:50176
	ds_read_b128 v[192:195], v150 offset:51200
	ds_read_b128 v[196:199], v150 offset:52224
	ds_read_b128 v[202:205], v150 offset:53248
	ds_read_b128 v[206:209], v150 offset:54272
	ds_read_b128 v[210:213], v150 offset:55296
	ds_read_b128 v[214:217], v150 offset:56320
	global_load_lds_dwordx4 v[218:219], off
	s_add_i32 m0, s28, 0x2000
	s_add_u32 s24, s24, 0x80080
	v_lshl_add_u64 v[218:219], v[220:221], 0, s[0:1]
	s_addc_u32 s25, s25, 0
	s_add_i32 s28, s51, s33
	global_load_lds_dwordx4 v[218:219], off
	v_lshl_add_u64 v[218:219], s[24:25], 0, v[136:137]
	s_mov_b32 m0, s28
	s_nop 0
	global_load_lds_dwordx4 v[218:219], off
	v_lshl_add_u64 v[218:219], s[24:25], 0, v[140:141]
	s_add_i32 m0, s28, 0x2000
	s_nop 0
	global_load_lds_dwordx4 v[218:219], off
	v_lshl_add_u64 v[218:219], v[222:223], 0, s[0:1]
	s_mov_b32 m0, s42
	s_nop 0
	global_load_lds_dwordx4 v[218:219], off
	v_lshl_add_u64 v[218:219], v[224:225], 0, s[0:1]
	s_mov_b32 m0, s43
	s_nop 0
	global_load_lds_dwordx4 v[218:219], off
	s_waitcnt vmcnt(8)
	s_waitcnt lgkmcnt(0)
	s_barrier
	s_waitcnt lgkmcnt(0)
	v_mfma_f32_16x16x32_bf16 v[54:57], v[152:155], v[184:187], v[54:57]
	v_mfma_f32_16x16x32_bf16 v[78:81], v[160:163], v[184:187], v[78:81]
	v_mfma_f32_16x16x32_bf16 v[62:65], v[152:155], v[192:195], v[62:65]
	v_mfma_f32_16x16x32_bf16 v[82:85], v[160:163], v[192:195], v[82:85]
	v_mfma_f32_16x16x32_bf16 v[70:73], v[152:155], v[202:205], v[70:73]
	v_mfma_f32_16x16x32_bf16 v[98:101], v[160:163], v[202:205], v[98:101]
	v_mfma_f32_16x16x32_bf16 v[90:93], v[152:155], v[210:213], v[90:93]
	v_mfma_f32_16x16x32_bf16 v[94:97], v[160:163], v[210:213], v[94:97]
	v_mfma_f32_16x16x32_bf16 v[54:57], v[156:159], v[188:191], v[54:57]
	v_mfma_f32_16x16x32_bf16 v[78:81], v[164:167], v[188:191], v[78:81]
	v_mfma_f32_16x16x32_bf16 v[62:65], v[156:159], v[196:199], v[62:65]
	v_mfma_f32_16x16x32_bf16 v[82:85], v[164:167], v[196:199], v[82:85]
	v_mfma_f32_16x16x32_bf16 v[70:73], v[156:159], v[206:209], v[70:73]
	v_mfma_f32_16x16x32_bf16 v[98:101], v[164:167], v[206:209], v[98:101]
	v_mfma_f32_16x16x32_bf16 v[90:93], v[156:159], v[214:217], v[90:93]
	v_mfma_f32_16x16x32_bf16 v[94:97], v[164:167], v[214:217], v[94:97]
	v_mfma_f32_16x16x32_bf16 v[114:117], v[168:171], v[184:187], v[114:117]
	v_mfma_f32_16x16x32_bf16 v[130:133], v[176:179], v[184:187], v[130:133]
	v_mfma_f32_16x16x32_bf16 v[110:113], v[168:171], v[192:195], v[110:113]
	v_mfma_f32_16x16x32_bf16 v[126:129], v[176:179], v[192:195], v[126:129]
	v_mfma_f32_16x16x32_bf16 v[106:109], v[168:171], v[202:205], v[106:109]
	v_mfma_f32_16x16x32_bf16 v[122:125], v[176:179], v[202:205], v[122:125]
	v_mfma_f32_16x16x32_bf16 v[102:105], v[168:171], v[210:213], v[102:105]
	v_mfma_f32_16x16x32_bf16 v[118:121], v[176:179], v[210:213], v[118:121]
	v_mfma_f32_16x16x32_bf16 v[114:117], v[172:175], v[188:191], v[114:117]
	v_mfma_f32_16x16x32_bf16 v[130:133], v[180:183], v[188:191], v[130:133]
	v_mfma_f32_16x16x32_bf16 v[110:113], v[172:175], v[196:199], v[110:113]
	v_mfma_f32_16x16x32_bf16 v[126:129], v[180:183], v[196:199], v[126:129]
	v_mfma_f32_16x16x32_bf16 v[106:109], v[172:175], v[206:209], v[106:109]
	v_mfma_f32_16x16x32_bf16 v[122:125], v[180:183], v[206:209], v[122:125]
	v_mfma_f32_16x16x32_bf16 v[102:105], v[172:175], v[214:217], v[102:105]
	v_mfma_f32_16x16x32_bf16 v[118:121], v[180:183], v[214:217], v[118:121]
	s_barrier
	s_add_i32 s49, s49, 2
	s_cmp_gt_u32 s49, 29
	s_mov_b64 s[28:29], s[22:23]
	s_cbranch_scc0 .LBB0_1128
	s_and_b64 vcc, exec, s[12:13]
	s_cbranch_vccz .LBB0_1131
	s_barrier

; #define PG8_STAGE_A(bufoff, base_, nx_, kb_, h_) do { if (GATHER) { if (nx_) PG8_STAGE_G(bufoff, kb_, goN, h_); else PG8_STAGE_G(bufoff, kb_, goC, h_); } \
;         else PG8_STAGE(bufoff, (base_) + (kb_) + (h_) * hstep, voffA); } while (0)
; #define PG8_STAGE(bufoff, gbase, voff) do { _Pragma("unroll") for (int _i = 0; _i < 2; ++_i) \
;         __builtin_amdgcn_global_load_lds((const unsigned*)((const char*)(gbase) + (voff)[_i]), (LAS unsigned*)(lds + (bufoff) + ldsw + _i * 8192), 16, 0, 0); } while (0)
; #define PG8_LDA(dst, b, h) do { _Pragma("unroll") for (int m = 0; m < 4; ++m) _Pragma("unroll") for (int k = 0; k < 2; ++k) dst[m][k] = *(const LAS bf16x8*)(lds + PG8_SA(b, h) + aoff + m * 2048 + k * 1024); } while (0)
; #define PG8_LDB(dst, b, h) do { _Pragma("unroll") for (int n = 0; n < 2; ++n) _Pragma("unroll") for (int k = 0; k < 2; ++k) dst[n][k] = *(const LAS bf16x8*)(lds + PG8_SB(b, h) + boff + n * 2048 + k * 1024); } while (0)
; #define PG8_MMA(ai, bj, At, Bt) do { __builtin_amdgcn_s_setprio(1); _Pragma("unroll") for (int m = 0; m < 4; ++m) _Pragma("unroll") for (int n = 0; n < 2; ++n) _Pragma("unroll") for (int k = 0; k < 2; ++k) \
;         acc[ai][bj][m][n] = __builtin_amdgcn_mfma_f32_16x16x32_bf16(Bt[n][k], At[m][k], acc[ai][bj][m][n], 0, 0, 0); __builtin_amdgcn_s_setprio(0); } while (0)
; #define PG8_WAIT_V(n) asm volatile("s_waitcnt vmcnt(" #n ")" ::: "memory")
; #define PG8_WAIT_L(n) asm volatile("s_waitcnt lgkmcnt(" #n ")" ::: "memory")
; #define PG8_BAR __builtin_amdgcn_s_barrier()
; #define PG8_SCHED __builtin_amdgcn_sched_barrier(0)
; template <class Epi, class Sched, bool GATHER = false>
; __device__ __forceinline__ void gemm_phase(LAS unsigned char* lds, const Gemm g, const Sched& S, const Epi& E, const int tid) {
;     ...
;             PG8_LDB(B0, 0, 0); PG8_LDB(B1, 0, 1); PG8_SCHED; PG8_LDA(At, 0, 0); PG8_STAGE_A(PG8_SA(1, 1), cA, false, kb1, 1);
;             PG8_WAIT_V(8); PG8_WAIT_L(0); PG8_BAR; PG8_MMA(0, 0, At, B0); PG8_MMA(0, 1, At, B1); PG8_BAR; PG8_SCHED;
;             PG8_LDA(At, 0, 1); PG8_STAGE(PG8_SB(0, 0), b2, voffB); PG8_STAGE(PG8_SB(0, 1), b2 + hstep, voffB); PG8_STAGE_A(PG8_SA(0, 0), (last ? nA : cA), last, kb2, 0);
;             PG8_WAIT_V(8); PG8_WAIT_L(0); PG8_BAR; PG8_MMA(1, 0, At, B0); PG8_MMA(1, 1, At, B1); PG8_BAR; PG8_SCHED;
.LBB0_1367:
	s_add_u32 s62, s59, s40
	s_addc_u32 s63, s60, s41
	s_add_u32 s36, s40, 0x100
	s_addc_u32 s37, s41, 0
	s_cmp_eq_u32 s61, 28
	s_cselect_b64 s[42:43], -1, 0
	s_and_b64 s[38:39], s[42:43], exec
	s_cselect_b32 s39, s21, s63
	s_cselect_b32 s38, s23, s62
	s_cselect_b32 s62, 0, s36
	s_add_i32 s63, 0, 0x10000
	v_add_u32_e32 v2, s63, v135
	s_add_i32 s64, 0, 0x14000
	ds_read_b128 v[152:155], v2
	ds_read_b128 v[156:159], v2 offset:1024
	ds_read_b128 v[160:163], v2 offset:2048
	ds_read_b128 v[164:167], v2 offset:3072
	v_add_u32_e32 v2, s64, v135
	ds_read_b128 v[168:171], v2
	ds_read_b128 v[172:175], v2 offset:1024
	ds_read_b128 v[176:179], v2 offset:2048
	ds_read_b128 v[180:183], v2 offset:3072
	v_lshl_add_u64 v[218:219], v[4:5], 0, s[40:41]
	s_add_i32 m0, s31, 0xc000
	ds_read_b128 v[184:187], v151
	ds_read_b128 v[188:191], v151 offset:1024
	ds_read_b128 v[192:195], v151 offset:2048
	ds_read_b128 v[196:199], v151 offset:3072
	ds_read_b128 v[202:205], v151 offset:4096
	ds_read_b128 v[206:209], v151 offset:5120
	ds_read_b128 v[210:213], v151 offset:6144
	ds_read_b128 v[214:217], v151 offset:7168
	global_load_lds_dwordx4 v[218:219], off
	v_lshl_add_u64 v[218:219], v[148:149], 0, s[40:41]
	s_add_i32 m0, s31, 0xe000
	s_nop 0
	global_load_lds_dwordx4 v[218:219], off
	s_waitcnt vmcnt(8)
	s_waitcnt lgkmcnt(0)
	s_barrier
	s_waitcnt lgkmcnt(0)
	v_mfma_f32_16x16x32_bf16 v[122:125], v[152:155], v[184:187], v[122:125]
	v_mfma_f32_16x16x32_bf16 v[74:77], v[160:163], v[184:187], v[74:77]
	v_mfma_f32_16x16x32_bf16 v[58:61], v[152:155], v[192:195], v[58:61]
	v_mfma_f32_16x16x32_bf16 v[50:53], v[160:163], v[192:195], v[50:53]
	v_mfma_f32_16x16x32_bf16 v[38:41], v[152:155], v[202:205], v[38:41]
	v_mfma_f32_16x16x32_bf16 v[34:37], v[160:163], v[202:205], v[34:37]
	v_mfma_f32_16x16x32_bf16 v[22:25], v[152:155], v[210:213], v[22:25]
	v_mfma_f32_16x16x32_bf16 v[18:21], v[160:163], v[210:213], v[18:21]
	v_mfma_f32_16x16x32_bf16 v[122:125], v[156:159], v[188:191], v[122:125]
	v_mfma_f32_16x16x32_bf16 v[74:77], v[164:167], v[188:191], v[74:77]
	v_mfma_f32_16x16x32_bf16 v[58:61], v[156:159], v[196:199], v[58:61]
	v_mfma_f32_16x16x32_bf16 v[50:53], v[164:167], v[196:199], v[50:53]
	v_mfma_f32_16x16x32_bf16 v[38:41], v[156:159], v[206:209], v[38:41]
	v_mfma_f32_16x16x32_bf16 v[34:37], v[164:167], v[206:209], v[34:37]
	v_mfma_f32_16x16x32_bf16 v[22:25], v[156:159], v[214:217], v[22:25]
	v_mfma_f32_16x16x32_bf16 v[18:21], v[164:167], v[214:217], v[18:21]
	v_mfma_f32_16x16x32_bf16 v[106:109], v[168:171], v[184:187], v[106:109]
	v_mfma_f32_16x16x32_bf16 v[110:113], v[176:179], v[184:187], v[110:113]
	v_mfma_f32_16x16x32_bf16 v[90:93], v[168:171], v[192:195], v[90:93]
	v_mfma_f32_16x16x32_bf16 v[94:97], v[176:179], v[192:195], v[94:97]
	v_mfma_f32_16x16x32_bf16 v[66:69], v[168:171], v[202:205], v[66:69]
	v_mfma_f32_16x16x32_bf16 v[70:73], v[176:179], v[202:205], v[70:73]
	v_mfma_f32_16x16x32_bf16 v[42:45], v[168:171], v[210:213], v[42:45]
	v_mfma_f32_16x16x32_bf16 v[46:49], v[176:179], v[210:213], v[46:49]
	v_mfma_f32_16x16x32_bf16 v[106:109], v[172:175], v[188:191], v[106:109]
	v_mfma_f32_16x16x32_bf16 v[110:113], v[180:183], v[188:191], v[110:113]
	v_mfma_f32_16x16x32_bf16 v[90:93], v[172:175], v[196:199], v[90:93]
	v_mfma_f32_16x16x32_bf16 v[94:97], v[180:183], v[196:199], v[94:97]
	v_mfma_f32_16x16x32_bf16 v[66:69], v[172:175], v[206:209], v[66:69]
	v_mfma_f32_16x16x32_bf16 v[70:73], v[180:183], v[206:209], v[70:73]
	v_mfma_f32_16x16x32_bf16 v[42:45], v[172:175], v[214:217], v[42:45]
	v_mfma_f32_16x16x32_bf16 v[46:49], v[180:183], v[214:217], v[46:49]
	s_barrier
	s_add_i32 s40, s63, s50
	v_lshl_add_u64 v[218:219], s[38:39], 0, v[140:141]
	s_mov_b32 m0, s40
	ds_read_b128 v[184:187], v151 offset:16384
	ds_read_b128 v[188:191], v151 offset:17408
	ds_read_b128 v[192:195], v151 offset:18432
	ds_read_b128 v[196:199], v151 offset:19456
	ds_read_b128 v[202:205], v151 offset:20480
	ds_read_b128 v[206:209], v151 offset:21504
	ds_read_b128 v[210:213], v151 offset:22528
	ds_read_b128 v[214:217], v151 offset:23552
	global_load_lds_dwordx4 v[218:219], off
	s_add_i32 m0, s40, 0x2000
	s_add_u32 s40, s38, 0x80000
	v_lshl_add_u64 v[220:221], s[38:39], 0, v[136:137]
	s_addc_u32 s41, s39, 0
	s_add_i32 s63, s64, s50
	global_load_lds_dwordx4 v[220:221], off
	v_lshl_add_u64 v[222:223], s[40:41], 0, v[140:141]
	s_mov_b32 m0, s63
	s_nop 0
	global_load_lds_dwordx4 v[222:223], off
	v_lshl_add_u64 v[222:223], s[40:41], 0, v[136:137]
	s_add_i32 m0, s63, 0x2000
	s_and_b64 s[40:41], s[8:9], s[42:43]
	s_and_b64 s[40:41], s[40:41], exec
	s_cselect_b32 s40, s24, s34
	s_cselect_b32 s41, s25, s35
	s_add_u32 s40, s40, s62
	s_addc_u32 s41, s41, 0
	global_load_lds_dwordx4 v[222:223], off
	v_lshl_add_u64 v[222:223], s[40:41], 0, v[142:143]
	s_mov_b32 m0, s31
	v_lshl_add_u64 v[224:225], s[40:41], 0, v[138:139]
	global_load_lds_dwordx4 v[222:223], off
	s_mov_b32 m0, s52
	s_nop 0
	global_load_lds_dwordx4 v[224:225], off
	s_waitcnt vmcnt(8)
	s_waitcnt lgkmcnt(0)
	s_barrier
; #define PG8_STAGE_A(bufoff, base_, nx_, kb_, h_) do { if (GATHER) { if (nx_) PG8_STAGE_G(bufoff, kb_, goN, h_); else PG8_STAGE_G(bufoff, kb_, goC, h_); } \
;         else PG8_STAGE(bufoff, (base_) + (kb_) + (h_) * hstep, voffA); } while (0)
; #define PG8_LDA(dst, b, h) do { _Pragma("unroll") for (int m = 0; m < 4; ++m) _Pragma("unroll") for (int k = 0; k < 2; ++k) dst[m][k] = *(const LAS bf16x8*)(lds + PG8_SA(b, h) + aoff + m * 2048 + k * 1024); } while (0)
; #define PG8_LDB(dst, b, h) do { _Pragma("unroll") for (int n = 0; n < 2; ++n) _Pragma("unroll") for (int k = 0; k < 2; ++k) dst[n][k] = *(const LAS bf16x8*)(lds + PG8_SB(b, h) + boff + n * 2048 + k * 1024); } while (0)
; #define PG8_MMA(ai, bj, At, Bt) do { __builtin_amdgcn_s_setprio(1); _Pragma("unroll") for (int m = 0; m < 4; ++m) _Pragma("unroll") for (int n = 0; n < 2; ++n) _Pragma("unroll") for (int k = 0; k < 2; ++k) \
;         acc[ai][bj][m][n] = __builtin_amdgcn_mfma_f32_16x16x32_bf16(Bt[n][k], At[m][k], acc[ai][bj][m][n], 0, 0, 0); __builtin_amdgcn_s_setprio(0); } while (0)
; #define PG8_WAIT_V(n) asm volatile("s_waitcnt vmcnt(" #n ")" ::: "memory")
; #define PG8_WAIT_L(n) asm volatile("s_waitcnt lgkmcnt(" #n ")" ::: "memory")
; #define PG8_BAR __builtin_amdgcn_s_barrier()
; #define PG8_SCHED __builtin_amdgcn_sched_barrier(0)
; template <class Epi, class Sched, bool GATHER = false>
; __device__ __forceinline__ void gemm_phase(LAS unsigned char* lds, const Gemm g, const Sched& S, const Epi& E, const int tid) {
;     ...
;             PG8_WAIT_V(8); PG8_WAIT_L(0); PG8_BAR; PG8_MMA(1, 0, At, B0); PG8_MMA(1, 1, At, B1); PG8_BAR; PG8_SCHED;
;             PG8_LDB(B0, 1, 0); PG8_LDB(B1, 1, 1); PG8_SCHED; PG8_LDA(At, 1, 0); PG8_STAGE_A(PG8_SA(0, 1), (last ? nA : cA), last, kb2, 1);
;             PG8_WAIT_V(8); PG8_WAIT_L(0); PG8_BAR; PG8_MMA(0, 0, At, B0); PG8_MMA(0, 1, At, B1); PG8_BAR; PG8_SCHED;
	s_waitcnt lgkmcnt(0)
	v_mfma_f32_16x16x32_bf16 v[30:33], v[152:155], v[184:187], v[30:33]
	v_mfma_f32_16x16x32_bf16 v[26:29], v[160:163], v[184:187], v[26:29]
	v_mfma_f32_16x16x32_bf16 v[14:17], v[152:155], v[192:195], v[14:17]
	v_mfma_f32_16x16x32_bf16 v[10:13], v[160:163], v[192:195], v[10:13]
	v_mfma_f32_16x16x32_bf16 v[6:9], v[152:155], v[202:205], v[6:9]
	v_mfma_f32_16x16x32_bf16 v[78:81], v[160:163], v[202:205], v[78:81]
	v_mfma_f32_16x16x32_bf16 v[62:65], v[152:155], v[210:213], v[62:65]
	v_mfma_f32_16x16x32_bf16 v[54:57], v[160:163], v[210:213], v[54:57]
	v_mfma_f32_16x16x32_bf16 v[30:33], v[156:159], v[188:191], v[30:33]
	v_mfma_f32_16x16x32_bf16 v[26:29], v[164:167], v[188:191], v[26:29]
	v_mfma_f32_16x16x32_bf16 v[14:17], v[156:159], v[196:199], v[14:17]
	v_mfma_f32_16x16x32_bf16 v[10:13], v[164:167], v[196:199], v[10:13]
	v_mfma_f32_16x16x32_bf16 v[6:9], v[156:159], v[206:209], v[6:9]
	v_mfma_f32_16x16x32_bf16 v[78:81], v[164:167], v[206:209], v[78:81]
	v_mfma_f32_16x16x32_bf16 v[62:65], v[156:159], v[214:217], v[62:65]
	v_mfma_f32_16x16x32_bf16 v[54:57], v[164:167], v[214:217], v[54:57]
	v_mfma_f32_16x16x32_bf16 v[130:133], v[168:171], v[184:187], v[130:133]
	v_mfma_f32_16x16x32_bf16 v[126:129], v[176:179], v[184:187], v[126:129]
	v_mfma_f32_16x16x32_bf16 v[118:121], v[168:171], v[192:195], v[118:121]
	v_mfma_f32_16x16x32_bf16 v[114:117], v[176:179], v[192:195], v[114:117]
	v_mfma_f32_16x16x32_bf16 v[102:105], v[168:171], v[202:205], v[102:105]
	v_mfma_f32_16x16x32_bf16 v[98:101], v[176:179], v[202:205], v[98:101]
	v_mfma_f32_16x16x32_bf16 v[86:89], v[168:171], v[210:213], v[86:89]
	v_mfma_f32_16x16x32_bf16 v[82:85], v[176:179], v[210:213], v[82:85]
	v_mfma_f32_16x16x32_bf16 v[130:133], v[172:175], v[188:191], v[130:133]
	v_mfma_f32_16x16x32_bf16 v[126:129], v[180:183], v[188:191], v[126:129]
	v_mfma_f32_16x16x32_bf16 v[118:121], v[172:175], v[196:199], v[118:121]
	v_mfma_f32_16x16x32_bf16 v[114:117], v[180:183], v[196:199], v[114:117]
	v_mfma_f32_16x16x32_bf16 v[102:105], v[172:175], v[206:209], v[102:105]
	v_mfma_f32_16x16x32_bf16 v[98:101], v[180:183], v[206:209], v[98:101]
	v_mfma_f32_16x16x32_bf16 v[86:89], v[172:175], v[214:217], v[86:89]
	v_mfma_f32_16x16x32_bf16 v[82:85], v[180:183], v[214:217], v[82:85]
	s_barrier
	s_add_i32 s42, 0, 0x18000
	v_add_u32_e32 v2, s42, v135
	s_add_i32 s43, 0, 0x1c000
	ds_read_b128 v[152:155], v2
	ds_read_b128 v[156:159], v2 offset:1024
	ds_read_b128 v[160:163], v2 offset:2048
	ds_read_b128 v[164:167], v2 offset:3072
	v_add_u32_e32 v2, s43, v135
	ds_read_b128 v[168:171], v2
	ds_read_b128 v[172:175], v2 offset:1024
	ds_read_b128 v[176:179], v2 offset:2048
	ds_read_b128 v[180:183], v2 offset:3072
	s_add_u32 s40, s40, 0x80000
	s_addc_u32 s41, s41, 0
	s_mov_b32 m0, s53
	v_lshl_add_u64 v[226:227], s[40:41], 0, v[142:143]
	ds_read_b128 v[184:187], v151 offset:32768
	ds_read_b128 v[188:191], v151 offset:33792
	ds_read_b128 v[192:195], v151 offset:34816
	ds_read_b128 v[196:199], v151 offset:35840
	ds_read_b128 v[202:205], v151 offset:36864
	ds_read_b128 v[206:209], v151 offset:37888
	ds_read_b128 v[210:213], v151 offset:38912
	ds_read_b128 v[214:217], v151 offset:39936
	global_load_lds_dwordx4 v[226:227], off
	v_lshl_add_u64 v[226:227], s[40:41], 0, v[138:139]
	s_mov_b32 m0, s54
	s_nop 0
	global_load_lds_dwordx4 v[226:227], off
	s_waitcnt vmcnt(8)
	s_waitcnt lgkmcnt(0)
	s_barrier
	s_waitcnt lgkmcnt(0)
	v_mfma_f32_16x16x32_bf16 v[122:125], v[152:155], v[184:187], v[122:125]
	v_mfma_f32_16x16x32_bf16 v[74:77], v[160:163], v[184:187], v[74:77]
	v_mfma_f32_16x16x32_bf16 v[58:61], v[152:155], v[192:195], v[58:61]
	v_mfma_f32_16x16x32_bf16 v[50:53], v[160:163], v[192:195], v[50:53]
	v_mfma_f32_16x16x32_bf16 v[38:41], v[152:155], v[202:205], v[38:41]
	v_mfma_f32_16x16x32_bf16 v[34:37], v[160:163], v[202:205], v[34:37]
	v_mfma_f32_16x16x32_bf16 v[22:25], v[152:155], v[210:213], v[22:25]
	v_mfma_f32_16x16x32_bf16 v[18:21], v[160:163], v[210:213], v[18:21]
	v_mfma_f32_16x16x32_bf16 v[122:125], v[156:159], v[188:191], v[122:125]
	v_mfma_f32_16x16x32_bf16 v[74:77], v[164:167], v[188:191], v[74:77]
	v_mfma_f32_16x16x32_bf16 v[58:61], v[156:159], v[196:199], v[58:61]
	v_mfma_f32_16x16x32_bf16 v[50:53], v[164:167], v[196:199], v[50:53]
	v_mfma_f32_16x16x32_bf16 v[38:41], v[156:159], v[206:209], v[38:41]
	v_mfma_f32_16x16x32_bf16 v[34:37], v[164:167], v[206:209], v[34:37]
	v_mfma_f32_16x16x32_bf16 v[22:25], v[156:159], v[214:217], v[22:25]
	v_mfma_f32_16x16x32_bf16 v[18:21], v[164:167], v[214:217], v[18:21]
	v_mfma_f32_16x16x32_bf16 v[106:109], v[168:171], v[184:187], v[106:109]
	v_mfma_f32_16x16x32_bf16 v[110:113], v[176:179], v[184:187], v[110:113]
	v_mfma_f32_16x16x32_bf16 v[90:93], v[168:171], v[192:195], v[90:93]
	v_mfma_f32_16x16x32_bf16 v[94:97], v[176:179], v[192:195], v[94:97]
	v_mfma_f32_16x16x32_bf16 v[66:69], v[168:171], v[202:205], v[66:69]
	v_mfma_f32_16x16x32_bf16 v[70:73], v[176:179], v[202:205], v[70:73]
	v_mfma_f32_16x16x32_bf16 v[42:45], v[168:171], v[210:213], v[42:45]
	v_mfma_f32_16x16x32_bf16 v[46:49], v[176:179], v[210:213], v[46:49]
	v_mfma_f32_16x16x32_bf16 v[106:109], v[172:175], v[188:191], v[106:109]
	v_mfma_f32_16x16x32_bf16 v[110:113], v[180:183], v[188:191], v[110:113]
	v_mfma_f32_16x16x32_bf16 v[90:93], v[172:175], v[196:199], v[90:93]
	v_mfma_f32_16x16x32_bf16 v[94:97], v[180:183], v[196:199], v[94:97]
	v_mfma_f32_16x16x32_bf16 v[66:69], v[172:175], v[206:209], v[66:69]
	v_mfma_f32_16x16x32_bf16 v[70:73], v[180:183], v[206:209], v[70:73]
	v_mfma_f32_16x16x32_bf16 v[42:45], v[172:175], v[214:217], v[42:45]
	v_mfma_f32_16x16x32_bf16 v[46:49], v[180:183], v[214:217], v[46:49]
	s_barrier
; #define PG8_STAGE_A(bufoff, base_, nx_, kb_, h_) do { if (GATHER) { if (nx_) PG8_STAGE_G(bufoff, kb_, goN, h_); else PG8_STAGE_G(bufoff, kb_, goC, h_); } \
;         else PG8_STAGE(bufoff, (base_) + (kb_) + (h_) * hstep, voffA); } while (0)
; #define PG8_STAGE(bufoff, gbase, voff) do { _Pragma("unroll") for (int _i = 0; _i < 2; ++_i) \
;         __builtin_amdgcn_global_load_lds((const unsigned*)((const char*)(gbase) + (voff)[_i]), (LAS unsigned*)(lds + (bufoff) + ldsw + _i * 8192), 16, 0, 0); } while (0)
; #define PG8_LDA(dst, b, h) do { _Pragma("unroll") for (int m = 0; m < 4; ++m) _Pragma("unroll") for (int k = 0; k < 2; ++k) dst[m][k] = *(const LAS bf16x8*)(lds + PG8_SA(b, h) + aoff + m * 2048 + k * 1024); } while (0)
; #define PG8_MMA(ai, bj, At, Bt) do { __builtin_amdgcn_s_setprio(1); _Pragma("unroll") for (int m = 0; m < 4; ++m) _Pragma("unroll") for (int n = 0; n < 2; ++n) _Pragma("unroll") for (int k = 0; k < 2; ++k) \
;         acc[ai][bj][m][n] = __builtin_amdgcn_mfma_f32_16x16x32_bf16(Bt[n][k], At[m][k], acc[ai][bj][m][n], 0, 0, 0); __builtin_amdgcn_s_setprio(0); } while (0)
; #define PG8_WAIT_V(n) asm volatile("s_waitcnt vmcnt(" #n ")" ::: "memory")
; #define PG8_WAIT_L(n) asm volatile("s_waitcnt lgkmcnt(" #n ")" ::: "memory")
; #define PG8_BAR __builtin_amdgcn_s_barrier()
; #define PG8_SCHED __builtin_amdgcn_sched_barrier(0)
; template <class Epi, class Sched, bool GATHER = false>
; __device__ __forceinline__ void gemm_phase(LAS unsigned char* lds, const Gemm g, const Sched& S, const Epi& E, const int tid) {
;     ...
;             PG8_LDA(At, 1, 1); PG8_STAGE(PG8_SB(1, 0), b3, voffB); PG8_STAGE(PG8_SB(1, 1), b3 + hstep, voffB); PG8_STAGE_A(PG8_SA(1, 0), (last ? nA : cA), last, kb3, 0);
;             PG8_WAIT_V(8); PG8_WAIT_L(0); PG8_BAR; PG8_MMA(1, 0, At, B0); PG8_MMA(1, 1, At, B1); PG8_BAR; PG8_SCHED;
	s_add_i32 s40, s42, s50
	v_lshl_add_u64 v[218:219], v[218:219], 0, s[0:1]
	s_mov_b32 m0, s40
	ds_read_b128 v[184:187], v151 offset:49152
	ds_read_b128 v[188:191], v151 offset:50176
	ds_read_b128 v[192:195], v151 offset:51200
	ds_read_b128 v[196:199], v151 offset:52224
	ds_read_b128 v[202:205], v151 offset:53248
	ds_read_b128 v[206:209], v151 offset:54272
	ds_read_b128 v[210:213], v151 offset:55296
	ds_read_b128 v[214:217], v151 offset:56320
	global_load_lds_dwordx4 v[218:219], off
	s_add_i32 m0, s40, 0x2000
	s_add_u32 s38, s38, 0x80080
	v_lshl_add_u64 v[218:219], v[220:221], 0, s[0:1]
	s_addc_u32 s39, s39, 0
	s_add_i32 s40, s43, s50
	global_load_lds_dwordx4 v[218:219], off
	v_lshl_add_u64 v[218:219], s[38:39], 0, v[140:141]
	s_mov_b32 m0, s40
	s_nop 0
	global_load_lds_dwordx4 v[218:219], off
	v_lshl_add_u64 v[218:219], s[38:39], 0, v[136:137]
	s_add_i32 m0, s40, 0x2000
	s_nop 0
	global_load_lds_dwordx4 v[218:219], off
	v_lshl_add_u64 v[218:219], v[222:223], 0, s[0:1]
	s_mov_b32 m0, s33
	s_nop 0
	global_load_lds_dwordx4 v[218:219], off
	v_lshl_add_u64 v[218:219], v[224:225], 0, s[0:1]
	s_mov_b32 m0, s55
	s_nop 0
	global_load_lds_dwordx4 v[218:219], off
	s_waitcnt vmcnt(8)
	s_waitcnt lgkmcnt(0)
	s_barrier
	s_waitcnt lgkmcnt(0)
	v_mfma_f32_16x16x32_bf16 v[30:33], v[152:155], v[184:187], v[30:33]
	v_mfma_f32_16x16x32_bf16 v[26:29], v[160:163], v[184:187], v[26:29]
	v_mfma_f32_16x16x32_bf16 v[14:17], v[152:155], v[192:195], v[14:17]
	v_mfma_f32_16x16x32_bf16 v[10:13], v[160:163], v[192:195], v[10:13]
	v_mfma_f32_16x16x32_bf16 v[6:9], v[152:155], v[202:205], v[6:9]
	v_mfma_f32_16x16x32_bf16 v[78:81], v[160:163], v[202:205], v[78:81]
	v_mfma_f32_16x16x32_bf16 v[62:65], v[152:155], v[210:213], v[62:65]
	v_mfma_f32_16x16x32_bf16 v[54:57], v[160:163], v[210:213], v[54:57]
	v_mfma_f32_16x16x32_bf16 v[30:33], v[156:159], v[188:191], v[30:33]
	v_mfma_f32_16x16x32_bf16 v[26:29], v[164:167], v[188:191], v[26:29]
	v_mfma_f32_16x16x32_bf16 v[14:17], v[156:159], v[196:199], v[14:17]
	v_mfma_f32_16x16x32_bf16 v[10:13], v[164:167], v[196:199], v[10:13]
	v_mfma_f32_16x16x32_bf16 v[6:9], v[156:159], v[206:209], v[6:9]
	v_mfma_f32_16x16x32_bf16 v[78:81], v[164:167], v[206:209], v[78:81]
	v_mfma_f32_16x16x32_bf16 v[62:65], v[156:159], v[214:217], v[62:65]
	v_mfma_f32_16x16x32_bf16 v[54:57], v[164:167], v[214:217], v[54:57]
	v_mfma_f32_16x16x32_bf16 v[130:133], v[168:171], v[184:187], v[130:133]
	v_mfma_f32_16x16x32_bf16 v[126:129], v[176:179], v[184:187], v[126:129]
	v_mfma_f32_16x16x32_bf16 v[118:121], v[168:171], v[192:195], v[118:121]
	v_mfma_f32_16x16x32_bf16 v[114:117], v[176:179], v[192:195], v[114:117]
	v_mfma_f32_16x16x32_bf16 v[102:105], v[168:171], v[202:205], v[102:105]
	v_mfma_f32_16x16x32_bf16 v[98:101], v[176:179], v[202:205], v[98:101]
	v_mfma_f32_16x16x32_bf16 v[86:89], v[168:171], v[210:213], v[86:89]
	v_mfma_f32_16x16x32_bf16 v[82:85], v[176:179], v[210:213], v[82:85]
	v_mfma_f32_16x16x32_bf16 v[130:133], v[172:175], v[188:191], v[130:133]
	v_mfma_f32_16x16x32_bf16 v[126:129], v[180:183], v[188:191], v[126:129]
	v_mfma_f32_16x16x32_bf16 v[118:121], v[172:175], v[196:199], v[118:121]
	v_mfma_f32_16x16x32_bf16 v[114:117], v[180:183], v[196:199], v[114:117]
	v_mfma_f32_16x16x32_bf16 v[102:105], v[172:175], v[206:209], v[102:105]
	v_mfma_f32_16x16x32_bf16 v[98:101], v[180:183], v[206:209], v[98:101]
	v_mfma_f32_16x16x32_bf16 v[86:89], v[172:175], v[214:217], v[86:89]
	v_mfma_f32_16x16x32_bf16 v[82:85], v[180:183], v[214:217], v[82:85]
	s_barrier
	s_add_i32 s61, s61, 2
	s_cmp_gt_u32 s61, 29
	s_mov_b64 s[40:41], s[36:37]
	s_cbranch_scc0 .LBB0_1367
	s_and_b64 vcc, exec, s[16:17]
	s_cbranch_vccz .LBB0_1370
	s_barrier

; #define PG8_STAGE_A(bufoff, base_, nx_, kb_, h_) do { if (GATHER) { if (nx_) PG8_STAGE_G(bufoff, kb_, goN, h_); else PG8_STAGE_G(bufoff, kb_, goC, h_); } \
;         else PG8_STAGE(bufoff, (base_) + (kb_) + (h_) * hstep, voffA); } while (0)
; #define PG8_LDA(dst, b, h) do { _Pragma("unroll") for (int m = 0; m < 4; ++m) _Pragma("unroll") for (int k = 0; k < 2; ++k) dst[m][k] = *(const LAS bf16x8*)(lds + PG8_SA(b, h) + aoff + m * 2048 + k * 1024); } while (0)
; #define PG8_LDB(dst, b, h) do { _Pragma("unroll") for (int n = 0; n < 2; ++n) _Pragma("unroll") for (int k = 0; k < 2; ++k) dst[n][k] = *(const LAS bf16x8*)(lds + PG8_SB(b, h) + boff + n * 2048 + k * 1024); } while (0)
; #define PG8_MMA(ai, bj, At, Bt) do { __builtin_amdgcn_s_setprio(1); _Pragma("unroll") for (int m = 0; m < 4; ++m) _Pragma("unroll") for (int n = 0; n < 2; ++n) _Pragma("unroll") for (int k = 0; k < 2; ++k) \
;         acc[ai][bj][m][n] = __builtin_amdgcn_mfma_f32_16x16x32_bf16(Bt[n][k], At[m][k], acc[ai][bj][m][n], 0, 0, 0); __builtin_amdgcn_s_setprio(0); } while (0)
; #define PG8_WAIT_V(n) asm volatile("s_waitcnt vmcnt(" #n ")" ::: "memory")
; #define PG8_WAIT_L(n) asm volatile("s_waitcnt lgkmcnt(" #n ")" ::: "memory")
; #define PG8_BAR __builtin_amdgcn_s_barrier()
; #define PG8_SCHED __builtin_amdgcn_sched_barrier(0)
; template <class Epi, class Sched, bool GATHER = false>
; __device__ __forceinline__ void gemm_phase(LAS unsigned char* lds, const Gemm g, const Sched& S, const Epi& E, const int tid) {
;     ...
;             PG8_LDB(B0, 0, 0); PG8_LDB(B1, 0, 1); PG8_SCHED; PG8_LDA(At, 0, 0); PG8_STAGE_A(PG8_SA(1, 1), cA, false, kb1, 1);
;             PG8_WAIT_V(8); PG8_WAIT_L(0); PG8_BAR; PG8_MMA(0, 0, At, B0); PG8_MMA(0, 1, At, B1); PG8_BAR; PG8_SCHED;
.LBB0_1397:
	s_add_u32 s30, s36, 0x100
	s_addc_u32 s31, s37, 0
	s_and_b64 s[72:73], s[10:11], exec
	s_cselect_b32 s71, 0, s30
	s_add_i32 s72, 0, 0x10000
	v_add_u32_e32 v2, s72, v219
	s_add_i32 s73, 0, 0x14000
	ds_read_b128 v[134:137], v2
	ds_read_b128 v[138:141], v2 offset:1024
	ds_read_b128 v[142:145], v2 offset:2048
	ds_read_b128 v[146:149], v2 offset:3072
	v_add_u32_e32 v2, s73, v219
	ds_read_b128 v[150:153], v2
	ds_read_b128 v[154:157], v2 offset:1024
	ds_read_b128 v[158:161], v2 offset:2048
	ds_read_b128 v[162:165], v2 offset:3072
	v_lshl_add_u64 v[4:5], v[226:227], 0, s[36:37]
	v_cndmask_b32_e64 v233, v5, v215, s[10:11]
	v_cndmask_b32_e64 v232, v4, v248, s[10:11]
	v_lshl_add_u64 v[4:5], v[230:231], 0, s[36:37]
	s_add_i32 m0, s58, 0xc000
	ds_read_b128 v[166:169], v249
	ds_read_b128 v[170:173], v249 offset:1024
	ds_read_b128 v[174:177], v249 offset:2048
	ds_read_b128 v[178:181], v249 offset:3072
	ds_read_b128 v[182:185], v249 offset:4096
	ds_read_b128 v[186:189], v249 offset:5120
	ds_read_b128 v[190:193], v249 offset:6144
	ds_read_b128 v[194:197], v249 offset:7168
	global_load_lds_dwordx4 v[4:5], off
	v_lshl_add_u64 v[4:5], v[228:229], 0, s[36:37]
	s_add_i32 m0, s58, 0xe000
	s_nop 0
	global_load_lds_dwordx4 v[4:5], off
	s_waitcnt vmcnt(8)
	s_waitcnt lgkmcnt(0)
	s_barrier
	s_waitcnt lgkmcnt(0)
	v_mfma_f32_16x16x32_bf16 v[130:133], v[134:137], v[166:169], v[130:133]
	v_mfma_f32_16x16x32_bf16 v[102:105], v[142:145], v[166:169], v[102:105]
	v_mfma_f32_16x16x32_bf16 v[82:85], v[134:137], v[174:177], v[82:85]
	v_mfma_f32_16x16x32_bf16 v[78:81], v[142:145], v[174:177], v[78:81]
	v_mfma_f32_16x16x32_bf16 v[54:57], v[134:137], v[182:185], v[54:57]
	v_mfma_f32_16x16x32_bf16 v[50:53], v[142:145], v[182:185], v[50:53]
	v_mfma_f32_16x16x32_bf16 v[22:25], v[134:137], v[190:193], v[22:25]
	v_mfma_f32_16x16x32_bf16 v[18:21], v[142:145], v[190:193], v[18:21]
	v_mfma_f32_16x16x32_bf16 v[130:133], v[138:141], v[170:173], v[130:133]
	v_mfma_f32_16x16x32_bf16 v[102:105], v[146:149], v[170:173], v[102:105]
	v_mfma_f32_16x16x32_bf16 v[82:85], v[138:141], v[178:181], v[82:85]
	v_mfma_f32_16x16x32_bf16 v[78:81], v[146:149], v[178:181], v[78:81]
	v_mfma_f32_16x16x32_bf16 v[54:57], v[138:141], v[186:189], v[54:57]
	v_mfma_f32_16x16x32_bf16 v[50:53], v[146:149], v[186:189], v[50:53]
	v_mfma_f32_16x16x32_bf16 v[22:25], v[138:141], v[194:197], v[22:25]
	v_mfma_f32_16x16x32_bf16 v[18:21], v[146:149], v[194:197], v[18:21]
	v_mfma_f32_16x16x32_bf16 v[122:125], v[150:153], v[166:169], v[122:125]
	v_mfma_f32_16x16x32_bf16 v[126:129], v[158:161], v[166:169], v[126:129]
	v_mfma_f32_16x16x32_bf16 v[106:109], v[150:153], v[174:177], v[106:109]
	v_mfma_f32_16x16x32_bf16 v[110:113], v[158:161], v[174:177], v[110:113]
	v_mfma_f32_16x16x32_bf16 v[86:89], v[150:153], v[182:185], v[86:89]
	v_mfma_f32_16x16x32_bf16 v[90:93], v[158:161], v[182:185], v[90:93]
	v_mfma_f32_16x16x32_bf16 v[58:61], v[150:153], v[190:193], v[58:61]
	v_mfma_f32_16x16x32_bf16 v[62:65], v[158:161], v[190:193], v[62:65]
	v_mfma_f32_16x16x32_bf16 v[122:125], v[154:157], v[170:173], v[122:125]
	v_mfma_f32_16x16x32_bf16 v[126:129], v[162:165], v[170:173], v[126:129]
	v_mfma_f32_16x16x32_bf16 v[106:109], v[154:157], v[178:181], v[106:109]
	v_mfma_f32_16x16x32_bf16 v[110:113], v[162:165], v[178:181], v[110:113]
	v_mfma_f32_16x16x32_bf16 v[86:89], v[154:157], v[186:189], v[86:89]
	v_mfma_f32_16x16x32_bf16 v[90:93], v[162:165], v[186:189], v[90:93]
	v_mfma_f32_16x16x32_bf16 v[58:61], v[154:157], v[194:197], v[58:61]
	v_mfma_f32_16x16x32_bf16 v[62:65], v[162:165], v[194:197], v[62:65]
	s_barrier
; #define PG8_STAGE_A(bufoff, base_, nx_, kb_, h_) do { if (GATHER) { if (nx_) PG8_STAGE_G(bufoff, kb_, goN, h_); else PG8_STAGE_G(bufoff, kb_, goC, h_); } \
;         else PG8_STAGE(bufoff, (base_) + (kb_) + (h_) * hstep, voffA); } while (0)
; #define PG8_STAGE(bufoff, gbase, voff) do { _Pragma("unroll") for (int _i = 0; _i < 2; ++_i) \
;         __builtin_amdgcn_global_load_lds((const unsigned*)((const char*)(gbase) + (voff)[_i]), (LAS unsigned*)(lds + (bufoff) + ldsw + _i * 8192), 16, 0, 0); } while (0)
; #define PG8_LDA(dst, b, h) do { _Pragma("unroll") for (int m = 0; m < 4; ++m) _Pragma("unroll") for (int k = 0; k < 2; ++k) dst[m][k] = *(const LAS bf16x8*)(lds + PG8_SA(b, h) + aoff + m * 2048 + k * 1024); } while (0)
; #define PG8_LDB(dst, b, h) do { _Pragma("unroll") for (int n = 0; n < 2; ++n) _Pragma("unroll") for (int k = 0; k < 2; ++k) dst[n][k] = *(const LAS bf16x8*)(lds + PG8_SB(b, h) + boff + n * 2048 + k * 1024); } while (0)
; #define PG8_MMA(ai, bj, At, Bt) do { __builtin_amdgcn_s_setprio(1); _Pragma("unroll") for (int m = 0; m < 4; ++m) _Pragma("unroll") for (int n = 0; n < 2; ++n) _Pragma("unroll") for (int k = 0; k < 2; ++k) \
;         acc[ai][bj][m][n] = __builtin_amdgcn_mfma_f32_16x16x32_bf16(Bt[n][k], At[m][k], acc[ai][bj][m][n], 0, 0, 0); __builtin_amdgcn_s_setprio(0); } while (0)
; #define PG8_WAIT_V(n) asm volatile("s_waitcnt vmcnt(" #n ")" ::: "memory")
; #define PG8_WAIT_L(n) asm volatile("s_waitcnt lgkmcnt(" #n ")" ::: "memory")
; #define PG8_BAR __builtin_amdgcn_s_barrier()
; #define PG8_SCHED __builtin_amdgcn_sched_barrier(0)
; template <class Epi, class Sched, bool GATHER = false>
; __device__ __forceinline__ void gemm_phase(LAS unsigned char* lds, const Gemm g, const Sched& S, const Epi& E, const int tid) {
;     ...
;             PG8_LDA(At, 0, 1); PG8_STAGE(PG8_SB(0, 0), b2, voffB); PG8_STAGE(PG8_SB(0, 1), b2 + hstep, voffB); PG8_STAGE_A(PG8_SA(0, 0), (last ? nA : cA), last, kb2, 0);
;             PG8_WAIT_V(8); PG8_WAIT_L(0); PG8_BAR; PG8_MMA(1, 0, At, B0); PG8_MMA(1, 1, At, B1); PG8_BAR; PG8_SCHED;
;             PG8_LDB(B0, 1, 0); PG8_LDB(B1, 1, 1); PG8_SCHED; PG8_LDA(At, 1, 0); PG8_STAGE_A(PG8_SA(0, 1), (last ? nA : cA), last, kb2, 1);
;             PG8_WAIT_V(8); PG8_WAIT_L(0); PG8_BAR; PG8_MMA(0, 0, At, B0); PG8_MMA(0, 1, At, B1); PG8_BAR; PG8_SCHED;
	s_add_i32 s36, s72, s57
	v_lshl_add_u64 v[234:235], v[232:233], 0, v[202:203]
	s_mov_b32 m0, s36
	ds_read_b128 v[166:169], v249 offset:16384
	ds_read_b128 v[170:173], v249 offset:17408
	ds_read_b128 v[174:177], v249 offset:18432
	ds_read_b128 v[178:181], v249 offset:19456
	ds_read_b128 v[182:185], v249 offset:20480
	ds_read_b128 v[186:189], v249 offset:21504
	ds_read_b128 v[190:193], v249 offset:22528
	ds_read_b128 v[194:197], v249 offset:23552
	global_load_lds_dwordx4 v[234:235], off
	s_add_i32 m0, s36, 0x2000
	s_mov_b64 s[36:37], 0x80000
	v_lshl_add_u64 v[236:237], v[232:233], 0, v[204:205]
	v_lshl_add_u64 v[4:5], v[232:233], 0, s[36:37]
	s_add_i32 s36, s73, s57
	global_load_lds_dwordx4 v[236:237], off
	v_lshl_add_u64 v[238:239], v[4:5], 0, v[202:203]
	s_mov_b32 m0, s36
	v_lshl_add_u64 v[4:5], v[4:5], 0, v[204:205]
	global_load_lds_dwordx4 v[238:239], off
	s_add_i32 m0, s36, 0x2000
	s_add_u32 s36, s12, s71
	s_addc_u32 s37, s13, 0
	v_cndmask_b32_e64 v2, v224, v206, s[10:11]
	global_load_lds_dwordx4 v[4:5], off
	v_lshl_add_u64 v[238:239], s[36:37], 0, v[2:3]
	s_mov_b32 m0, s58
	v_cndmask_b32_e64 v4, v218, v213, s[10:11]
	global_load_lds_dwordx4 v[238:239], off
	s_mov_b32 m0, s59
	s_nop 0
	global_load_lds_dwordx4 v4, s[36:37]
	s_waitcnt vmcnt(8)
	s_waitcnt lgkmcnt(0)
	s_barrier
	s_waitcnt lgkmcnt(0)
	v_mfma_f32_16x16x32_bf16 v[42:45], v[134:137], v[166:169], v[42:45]
	v_mfma_f32_16x16x32_bf16 v[26:29], v[142:145], v[166:169], v[26:29]
	v_mfma_f32_16x16x32_bf16 v[14:17], v[134:137], v[174:177], v[14:17]
	v_mfma_f32_16x16x32_bf16 v[66:69], v[142:145], v[174:177], v[66:69]
	v_mfma_f32_16x16x32_bf16 v[46:49], v[134:137], v[182:185], v[46:49]
	v_mfma_f32_16x16x32_bf16 v[30:33], v[142:145], v[182:185], v[30:33]
	v_mfma_f32_16x16x32_bf16 v[10:13], v[134:137], v[190:193], v[10:13]
	v_mfma_f32_16x16x32_bf16 v[4:7], v[142:145], v[190:193], v[6:9]
	v_mfma_f32_16x16x32_bf16 v[42:45], v[138:141], v[170:173], v[42:45]
	v_mfma_f32_16x16x32_bf16 v[26:29], v[146:149], v[170:173], v[26:29]
	v_mfma_f32_16x16x32_bf16 v[14:17], v[138:141], v[178:181], v[14:17]
	v_mfma_f32_16x16x32_bf16 v[66:69], v[146:149], v[178:181], v[66:69]
	v_mfma_f32_16x16x32_bf16 v[46:49], v[138:141], v[186:189], v[46:49]
	v_mfma_f32_16x16x32_bf16 v[30:33], v[146:149], v[186:189], v[30:33]
	v_mfma_f32_16x16x32_bf16 v[10:13], v[138:141], v[194:197], v[10:13]
	v_mfma_f32_16x16x32_bf16 v[4:7], v[146:149], v[194:197], v[4:7]
	v_mfma_f32_16x16x32_bf16 v[118:121], v[150:153], v[166:169], v[118:121]
	v_mfma_f32_16x16x32_bf16 v[114:117], v[158:161], v[166:169], v[114:117]
	v_mfma_f32_16x16x32_bf16 v[98:101], v[150:153], v[174:177], v[98:101]
	v_mfma_f32_16x16x32_bf16 v[94:97], v[158:161], v[174:177], v[94:97]
	v_mfma_f32_16x16x32_bf16 v[74:77], v[150:153], v[182:185], v[74:77]
	v_mfma_f32_16x16x32_bf16 v[70:73], v[158:161], v[182:185], v[70:73]
	v_mfma_f32_16x16x32_bf16 v[38:41], v[150:153], v[190:193], v[38:41]
	v_mfma_f32_16x16x32_bf16 v[34:37], v[158:161], v[190:193], v[34:37]
	v_mfma_f32_16x16x32_bf16 v[118:121], v[154:157], v[170:173], v[118:121]
	v_mfma_f32_16x16x32_bf16 v[114:117], v[162:165], v[170:173], v[114:117]
	v_mfma_f32_16x16x32_bf16 v[98:101], v[154:157], v[178:181], v[98:101]
	v_mfma_f32_16x16x32_bf16 v[94:97], v[162:165], v[178:181], v[94:97]
	v_mfma_f32_16x16x32_bf16 v[74:77], v[154:157], v[186:189], v[74:77]
	v_mfma_f32_16x16x32_bf16 v[70:73], v[162:165], v[186:189], v[70:73]
	v_mfma_f32_16x16x32_bf16 v[38:41], v[154:157], v[194:197], v[38:41]
	v_mfma_f32_16x16x32_bf16 v[34:37], v[162:165], v[194:197], v[34:37]
	s_barrier
	v_add_u32_e32 v2, 0, v219
	v_add_u32_e32 v8, 0x18000, v2
	v_add_u32_e32 v2, 0x1c000, v2
	ds_read_b128 v[150:153], v8
	ds_read_b128 v[154:157], v8 offset:1024
	ds_read_b128 v[158:161], v8 offset:2048
	ds_read_b128 v[162:165], v8 offset:3072
	ds_read_b128 v[134:137], v2
	ds_read_b128 v[138:141], v2 offset:1024
	ds_read_b128 v[142:145], v2 offset:2048
	ds_read_b128 v[146:149], v2 offset:3072
	ds_read_b128 v[190:193], v249 offset:32768
	ds_read_b128 v[194:197], v249 offset:33792
	ds_read_b128 v[182:185], v249 offset:34816
	ds_read_b128 v[186:189], v249 offset:35840
	ds_read_b128 v[174:177], v249 offset:36864
	ds_read_b128 v[178:181], v249 offset:37888
	ds_read_b128 v[166:169], v249 offset:38912
	ds_read_b128 v[170:173], v249 offset:39936
	s_andn2_b64 vcc, exec, s[34:35]
	s_cbranch_vccnz .LBB0_1399
	s_mov_b32 m0, s60
	v_lshl_add_u64 v[8:9], s[36:37], 0, v[220:221]
	global_load_lds_dwordx4 v[8:9], off
	v_mov_b64_e32 v[8:9], v[222:223]
	s_mov_b64 s[72:73], 0xb0000
	v_mov_b32_e32 v2, v218
	s_cbranch_execz .LBB0_1400
	s_branch .LBB0_1401

; #define PG8_STAGE_A(bufoff, base_, nx_, kb_, h_) do { if (GATHER) { if (nx_) PG8_STAGE_G(bufoff, kb_, goN, h_); else PG8_STAGE_G(bufoff, kb_, goC, h_); } \
;         else PG8_STAGE(bufoff, (base_) + (kb_) + (h_) * hstep, voffA); } while (0)
; #define PG8_STAGE(bufoff, gbase, voff) do { _Pragma("unroll") for (int _i = 0; _i < 2; ++_i) \
;         __builtin_amdgcn_global_load_lds((const unsigned*)((const char*)(gbase) + (voff)[_i]), (LAS unsigned*)(lds + (bufoff) + ldsw + _i * 8192), 16, 0, 0); } while (0)
; #define PG8_LDA(dst, b, h) do { _Pragma("unroll") for (int m = 0; m < 4; ++m) _Pragma("unroll") for (int k = 0; k < 2; ++k) dst[m][k] = *(const LAS bf16x8*)(lds + PG8_SA(b, h) + aoff + m * 2048 + k * 1024); } while (0)
; #define PG8_MMA(ai, bj, At, Bt) do { __builtin_amdgcn_s_setprio(1); _Pragma("unroll") for (int m = 0; m < 4; ++m) _Pragma("unroll") for (int n = 0; n < 2; ++n) _Pragma("unroll") for (int k = 0; k < 2; ++k) \
;         acc[ai][bj][m][n] = __builtin_amdgcn_mfma_f32_16x16x32_bf16(Bt[n][k], At[m][k], acc[ai][bj][m][n], 0, 0, 0); __builtin_amdgcn_s_setprio(0); } while (0)
; #define PG8_WAIT_V(n) asm volatile("s_waitcnt vmcnt(" #n ")" ::: "memory")
; #define PG8_WAIT_L(n) asm volatile("s_waitcnt lgkmcnt(" #n ")" ::: "memory")
; #define PG8_BAR __builtin_amdgcn_s_barrier()
; #define PG8_SCHED __builtin_amdgcn_sched_barrier(0)
; template <class Epi, class Sched, bool GATHER = false>
; __device__ __forceinline__ void gemm_phase(LAS unsigned char* lds, const Gemm g, const Sched& S, const Epi& E, const int tid) {
;     ...
;             PG8_WAIT_V(8); PG8_WAIT_L(0); PG8_BAR; PG8_MMA(0, 0, At, B0); PG8_MMA(0, 1, At, B1); PG8_BAR; PG8_SCHED;
;             PG8_LDA(At, 1, 1); PG8_STAGE(PG8_SB(1, 0), b3, voffB); PG8_STAGE(PG8_SB(1, 1), b3 + hstep, voffB); PG8_STAGE_A(PG8_SA(1, 0), (last ? nA : cA), last, kb3, 0);
;             PG8_WAIT_V(8); PG8_WAIT_L(0); PG8_BAR; PG8_MMA(1, 0, At, B0); PG8_MMA(1, 1, At, B1); PG8_BAR; PG8_SCHED;
;     ...
;         }
.LBB0_1401:
	v_lshl_add_u64 v[8:9], s[36:37], 0, v[8:9]
	s_mov_b32 m0, s61
	s_nop 0
	global_load_lds_dwordx4 v[8:9], off
	s_waitcnt vmcnt(8)
	s_waitcnt lgkmcnt(0)
	s_barrier
	s_waitcnt lgkmcnt(0)
	v_mfma_f32_16x16x32_bf16 v[130:133], v[150:153], v[190:193], v[130:133]
	v_mfma_f32_16x16x32_bf16 v[102:105], v[158:161], v[190:193], v[102:105]
	v_mfma_f32_16x16x32_bf16 v[82:85], v[150:153], v[182:185], v[82:85]
	v_mfma_f32_16x16x32_bf16 v[78:81], v[158:161], v[182:185], v[78:81]
	v_mfma_f32_16x16x32_bf16 v[54:57], v[150:153], v[174:177], v[54:57]
	v_mfma_f32_16x16x32_bf16 v[50:53], v[158:161], v[174:177], v[50:53]
	v_mfma_f32_16x16x32_bf16 v[22:25], v[150:153], v[166:169], v[22:25]
	v_mfma_f32_16x16x32_bf16 v[18:21], v[158:161], v[166:169], v[18:21]
	v_mfma_f32_16x16x32_bf16 v[130:133], v[154:157], v[194:197], v[130:133]
	v_mfma_f32_16x16x32_bf16 v[102:105], v[162:165], v[194:197], v[102:105]
	v_mfma_f32_16x16x32_bf16 v[82:85], v[154:157], v[186:189], v[82:85]
	v_mfma_f32_16x16x32_bf16 v[78:81], v[162:165], v[186:189], v[78:81]
	v_mfma_f32_16x16x32_bf16 v[54:57], v[154:157], v[178:181], v[54:57]
	v_mfma_f32_16x16x32_bf16 v[50:53], v[162:165], v[178:181], v[50:53]
	v_mfma_f32_16x16x32_bf16 v[22:25], v[154:157], v[170:173], v[22:25]
	v_mfma_f32_16x16x32_bf16 v[18:21], v[162:165], v[170:173], v[18:21]
	v_mfma_f32_16x16x32_bf16 v[122:125], v[134:137], v[190:193], v[122:125]
	v_mfma_f32_16x16x32_bf16 v[126:129], v[142:145], v[190:193], v[126:129]
	v_mfma_f32_16x16x32_bf16 v[106:109], v[134:137], v[182:185], v[106:109]
	v_mfma_f32_16x16x32_bf16 v[110:113], v[142:145], v[182:185], v[110:113]
	v_mfma_f32_16x16x32_bf16 v[86:89], v[134:137], v[174:177], v[86:89]
	v_mfma_f32_16x16x32_bf16 v[90:93], v[142:145], v[174:177], v[90:93]
	v_mfma_f32_16x16x32_bf16 v[58:61], v[134:137], v[166:169], v[58:61]
	v_mfma_f32_16x16x32_bf16 v[62:65], v[142:145], v[166:169], v[62:65]
	v_mfma_f32_16x16x32_bf16 v[122:125], v[138:141], v[194:197], v[122:125]
	v_mfma_f32_16x16x32_bf16 v[126:129], v[146:149], v[194:197], v[126:129]
	v_mfma_f32_16x16x32_bf16 v[106:109], v[138:141], v[186:189], v[106:109]
	v_mfma_f32_16x16x32_bf16 v[110:113], v[146:149], v[186:189], v[110:113]
	v_mfma_f32_16x16x32_bf16 v[86:89], v[138:141], v[178:181], v[86:89]
	v_mfma_f32_16x16x32_bf16 v[90:93], v[146:149], v[178:181], v[90:93]
	v_mfma_f32_16x16x32_bf16 v[58:61], v[138:141], v[170:173], v[58:61]
	v_mfma_f32_16x16x32_bf16 v[62:65], v[146:149], v[170:173], v[62:65]
	s_barrier
	s_mov_b32 m0, s62
	v_lshl_add_u64 v[8:9], v[234:235], 0, s[0:1]
	ds_read_b128 v[166:169], v249 offset:49152
	ds_read_b128 v[170:173], v249 offset:50176
	ds_read_b128 v[174:177], v249 offset:51200
	ds_read_b128 v[178:181], v249 offset:52224
	ds_read_b128 v[182:185], v249 offset:53248
	ds_read_b128 v[186:189], v249 offset:54272
	ds_read_b128 v[190:193], v249 offset:55296
	ds_read_b128 v[194:197], v249 offset:56320
	global_load_lds_dwordx4 v[8:9], off
	v_lshl_add_u64 v[8:9], v[236:237], 0, s[0:1]
	s_mov_b32 m0, s33
	s_mov_b64 s[10:11], 0x80080
	global_load_lds_dwordx4 v[8:9], off
	v_lshl_add_u64 v[8:9], v[232:233], 0, s[10:11]
	v_lshl_add_u64 v[232:233], v[8:9], 0, v[202:203]
	s_mov_b32 m0, s63
	v_lshl_add_u64 v[8:9], v[8:9], 0, v[204:205]
	global_load_lds_dwordx4 v[232:233], off
	s_mov_b32 m0, s64
	s_nop 0
	global_load_lds_dwordx4 v[8:9], off
	v_lshl_add_u64 v[8:9], v[238:239], 0, s[0:1]
	s_mov_b32 m0, s48
	s_nop 0
	global_load_lds_dwordx4 v[8:9], off
	v_lshl_add_u64 v[8:9], s[36:37], 0, v[2:3]
	v_lshl_add_u64 v[8:9], v[8:9], 0, s[0:1]
	s_mov_b32 m0, s49
	s_nop 0
	global_load_lds_dwordx4 v[8:9], off
	s_waitcnt vmcnt(8)
	s_waitcnt lgkmcnt(0)
	s_barrier
	s_waitcnt lgkmcnt(0)
	v_mfma_f32_16x16x32_bf16 v[42:45], v[150:153], v[166:169], v[42:45]
	v_mfma_f32_16x16x32_bf16 v[26:29], v[158:161], v[166:169], v[26:29]
	v_mfma_f32_16x16x32_bf16 v[14:17], v[150:153], v[174:177], v[14:17]
	v_mfma_f32_16x16x32_bf16 v[66:69], v[158:161], v[174:177], v[66:69]
	v_mfma_f32_16x16x32_bf16 v[46:49], v[150:153], v[182:185], v[46:49]
	v_mfma_f32_16x16x32_bf16 v[30:33], v[158:161], v[182:185], v[30:33]
	v_mfma_f32_16x16x32_bf16 v[8:11], v[150:153], v[190:193], v[10:13]
	v_mfma_f32_16x16x32_bf16 v[4:7], v[158:161], v[190:193], v[4:7]
	v_mfma_f32_16x16x32_bf16 v[42:45], v[154:157], v[170:173], v[42:45]
	v_mfma_f32_16x16x32_bf16 v[26:29], v[162:165], v[170:173], v[26:29]
	v_mfma_f32_16x16x32_bf16 v[14:17], v[154:157], v[178:181], v[14:17]
	v_mfma_f32_16x16x32_bf16 v[66:69], v[162:165], v[178:181], v[66:69]
	v_mfma_f32_16x16x32_bf16 v[46:49], v[154:157], v[186:189], v[46:49]
	v_mfma_f32_16x16x32_bf16 v[30:33], v[162:165], v[186:189], v[30:33]
	v_mfma_f32_16x16x32_bf16 v[10:13], v[154:157], v[194:197], v[8:11]
	v_mfma_f32_16x16x32_bf16 v[6:9], v[162:165], v[194:197], v[4:7]
	v_mfma_f32_16x16x32_bf16 v[118:121], v[134:137], v[166:169], v[118:121]
	v_mfma_f32_16x16x32_bf16 v[114:117], v[142:145], v[166:169], v[114:117]
	v_mfma_f32_16x16x32_bf16 v[98:101], v[134:137], v[174:177], v[98:101]
	v_mfma_f32_16x16x32_bf16 v[94:97], v[142:145], v[174:177], v[94:97]
	v_mfma_f32_16x16x32_bf16 v[74:77], v[134:137], v[182:185], v[74:77]
	v_mfma_f32_16x16x32_bf16 v[70:73], v[142:145], v[182:185], v[70:73]
	v_mfma_f32_16x16x32_bf16 v[38:41], v[134:137], v[190:193], v[38:41]
	v_mfma_f32_16x16x32_bf16 v[34:37], v[142:145], v[190:193], v[34:37]
	v_mfma_f32_16x16x32_bf16 v[118:121], v[138:141], v[170:173], v[118:121]
	v_mfma_f32_16x16x32_bf16 v[114:117], v[146:149], v[170:173], v[114:117]
	v_mfma_f32_16x16x32_bf16 v[98:101], v[138:141], v[178:181], v[98:101]
	v_mfma_f32_16x16x32_bf16 v[94:97], v[146:149], v[178:181], v[94:97]
	v_mfma_f32_16x16x32_bf16 v[74:77], v[138:141], v[186:189], v[74:77]
	v_mfma_f32_16x16x32_bf16 v[70:73], v[146:149], v[186:189], v[70:73]
	v_mfma_f32_16x16x32_bf16 v[38:41], v[138:141], v[194:197], v[38:41]
	v_mfma_f32_16x16x32_bf16 v[34:37], v[146:149], v[194:197], v[34:37]
	s_barrier
	s_add_i32 s70, s70, 2
	s_cmp_gt_u32 s70, 29
	s_cbranch_scc1 .LBB0_1403
	s_mov_b64 s[36:37], s[30:31]
	s_branch .LBB0_1395

; #define PG8_STAGE_A(bufoff, base_, nx_, kb_, h_) do { if (GATHER) { if (nx_) PG8_STAGE_G(bufoff, kb_, goN, h_); else PG8_STAGE_G(bufoff, kb_, goC, h_); } \
;         else PG8_STAGE(bufoff, (base_) + (kb_) + (h_) * hstep, voffA); } while (0)
; #define PG8_STAGE(bufoff, gbase, voff) do { _Pragma("unroll") for (int _i = 0; _i < 2; ++_i) \
;         __builtin_amdgcn_global_load_lds((const unsigned*)((const char*)(gbase) + (voff)[_i]), (LAS unsigned*)(lds + (bufoff) + ldsw + _i * 8192), 16, 0, 0); } while (0)
; #define PG8_LDA(dst, b, h) do { _Pragma("unroll") for (int m = 0; m < 4; ++m) _Pragma("unroll") for (int k = 0; k < 2; ++k) dst[m][k] = *(const LAS bf16x8*)(lds + PG8_SA(b, h) + aoff + m * 2048 + k * 1024); } while (0)
; #define PG8_LDB(dst, b, h) do { _Pragma("unroll") for (int n = 0; n < 2; ++n) _Pragma("unroll") for (int k = 0; k < 2; ++k) dst[n][k] = *(const LAS bf16x8*)(lds + PG8_SB(b, h) + boff + n * 2048 + k * 1024); } while (0)
; #define PG8_MMA(ai, bj, At, Bt) do { __builtin_amdgcn_s_setprio(1); _Pragma("unroll") for (int m = 0; m < 4; ++m) _Pragma("unroll") for (int n = 0; n < 2; ++n) _Pragma("unroll") for (int k = 0; k < 2; ++k) \
;         acc[ai][bj][m][n] = __builtin_amdgcn_mfma_f32_16x16x32_bf16(Bt[n][k], At[m][k], acc[ai][bj][m][n], 0, 0, 0); __builtin_amdgcn_s_setprio(0); } while (0)
; #define PG8_WAIT_V(n) asm volatile("s_waitcnt vmcnt(" #n ")" ::: "memory")
; #define PG8_WAIT_L(n) asm volatile("s_waitcnt lgkmcnt(" #n ")" ::: "memory")
; #define PG8_BAR __builtin_amdgcn_s_barrier()
; #define PG8_SCHED __builtin_amdgcn_sched_barrier(0)
; template <class Epi, class Sched, bool GATHER = false>
; __device__ __forceinline__ void gemm_phase(LAS unsigned char* lds, const Gemm g, const Sched& S, const Epi& E, const int tid) {
;     ...
;             PG8_LDB(B0, 0, 0); PG8_LDB(B1, 0, 1); PG8_SCHED; PG8_LDA(At, 0, 0); PG8_STAGE_A(PG8_SA(1, 1), cA, false, kb1, 1);
;             PG8_WAIT_V(8); PG8_WAIT_L(0); PG8_BAR; PG8_MMA(0, 0, At, B0); PG8_MMA(0, 1, At, B1); PG8_BAR; PG8_SCHED;
;             PG8_LDA(At, 0, 1); PG8_STAGE(PG8_SB(0, 0), b2, voffB); PG8_STAGE(PG8_SB(0, 1), b2 + hstep, voffB); PG8_STAGE_A(PG8_SA(0, 0), (last ? nA : cA), last, kb2, 0);
;             PG8_WAIT_V(8); PG8_WAIT_L(0); PG8_BAR; PG8_MMA(1, 0, At, B0); PG8_MMA(1, 1, At, B1); PG8_BAR; PG8_SCHED;
.LBB0_1483:
	s_add_u32 s28, s34, 0x100
	s_addc_u32 s29, s35, 0
	s_add_u32 s30, s56, s34
	s_addc_u32 s31, s57, s35
	s_add_i32 s59, 0, 0x10000
	s_add_i32 s60, 0, 0x14000
	v_add_u32_e32 v2, s59, v149
	ds_read_b128 v[152:155], v2
	ds_read_b128 v[156:159], v2 offset:1024
	ds_read_b128 v[160:163], v2 offset:2048
	ds_read_b128 v[164:167], v2 offset:3072
	v_add_u32_e32 v2, s60, v149
	ds_read_b128 v[168:171], v2
	ds_read_b128 v[172:175], v2 offset:1024
	ds_read_b128 v[176:179], v2 offset:2048
	ds_read_b128 v[180:183], v2 offset:3072
	s_add_i32 s62, s59, s33
	s_add_i32 m0, s44, 0xc000
	s_add_i32 s61, s44, 0xe000
	s_add_i32 s59, s62, 0x2000
	s_cmpk_eq_i32 s58, 0x54
	s_cselect_b32 s31, s25, s31
	s_cselect_b32 s30, s24, s30
	v_lshl_add_u64 v[218:219], v[4:5], 0, s[34:35]
	ds_read_b128 v[184:187], v151
	ds_read_b128 v[188:191], v151 offset:1024
	ds_read_b128 v[192:195], v151 offset:2048
	ds_read_b128 v[196:199], v151 offset:3072
	ds_read_b128 v[202:205], v151 offset:4096
	ds_read_b128 v[206:209], v151 offset:5120
	ds_read_b128 v[210:213], v151 offset:6144
	ds_read_b128 v[214:217], v151 offset:7168
	global_load_lds_dwordx4 v[218:219], off
	v_lshl_add_u64 v[218:219], v[146:147], 0, s[34:35]
	s_mov_b32 m0, s61
	s_nop 0
	global_load_lds_dwordx4 v[218:219], off
	s_waitcnt vmcnt(8)
	s_waitcnt lgkmcnt(0)
	s_barrier
	s_waitcnt lgkmcnt(0)
	v_mfma_f32_16x16x32_bf16 v[86:89], v[152:155], v[184:187], v[86:89]
	v_mfma_f32_16x16x32_bf16 v[18:21], v[160:163], v[184:187], v[18:21]
	v_mfma_f32_16x16x32_bf16 v[6:9], v[152:155], v[192:195], v[6:9]
	v_mfma_f32_16x16x32_bf16 v[22:25], v[160:163], v[192:195], v[22:25]
	v_mfma_f32_16x16x32_bf16 v[10:13], v[152:155], v[202:205], v[10:13]
	v_mfma_f32_16x16x32_bf16 v[26:29], v[160:163], v[202:205], v[26:29]
	v_mfma_f32_16x16x32_bf16 v[14:17], v[152:155], v[210:213], v[14:17]
	v_mfma_f32_16x16x32_bf16 v[30:33], v[160:163], v[210:213], v[30:33]
	v_mfma_f32_16x16x32_bf16 v[86:89], v[156:159], v[188:191], v[86:89]
	v_mfma_f32_16x16x32_bf16 v[18:21], v[164:167], v[188:191], v[18:21]
	v_mfma_f32_16x16x32_bf16 v[6:9], v[156:159], v[196:199], v[6:9]
	v_mfma_f32_16x16x32_bf16 v[22:25], v[164:167], v[196:199], v[22:25]
	v_mfma_f32_16x16x32_bf16 v[10:13], v[156:159], v[206:209], v[10:13]
	v_mfma_f32_16x16x32_bf16 v[26:29], v[164:167], v[206:209], v[26:29]
	v_mfma_f32_16x16x32_bf16 v[14:17], v[156:159], v[214:217], v[14:17]
	v_mfma_f32_16x16x32_bf16 v[30:33], v[164:167], v[214:217], v[30:33]
	v_mfma_f32_16x16x32_bf16 v[34:37], v[168:171], v[184:187], v[34:37]
	v_mfma_f32_16x16x32_bf16 v[50:53], v[176:179], v[184:187], v[50:53]
	v_mfma_f32_16x16x32_bf16 v[38:41], v[168:171], v[192:195], v[38:41]
	v_mfma_f32_16x16x32_bf16 v[54:57], v[176:179], v[192:195], v[54:57]
	v_mfma_f32_16x16x32_bf16 v[42:45], v[168:171], v[202:205], v[42:45]
	v_mfma_f32_16x16x32_bf16 v[62:65], v[176:179], v[202:205], v[62:65]
	v_mfma_f32_16x16x32_bf16 v[46:49], v[168:171], v[210:213], v[46:49]
	v_mfma_f32_16x16x32_bf16 v[70:73], v[176:179], v[210:213], v[70:73]
	v_mfma_f32_16x16x32_bf16 v[34:37], v[172:175], v[188:191], v[34:37]
	v_mfma_f32_16x16x32_bf16 v[50:53], v[180:183], v[188:191], v[50:53]
	v_mfma_f32_16x16x32_bf16 v[38:41], v[172:175], v[196:199], v[38:41]
	v_mfma_f32_16x16x32_bf16 v[54:57], v[180:183], v[196:199], v[54:57]
	v_mfma_f32_16x16x32_bf16 v[42:45], v[172:175], v[206:209], v[42:45]
	v_mfma_f32_16x16x32_bf16 v[62:65], v[180:183], v[206:209], v[62:65]
	v_mfma_f32_16x16x32_bf16 v[46:49], v[172:175], v[214:217], v[46:49]
	v_mfma_f32_16x16x32_bf16 v[70:73], v[180:183], v[214:217], v[70:73]
	s_barrier
	s_mov_b32 m0, s62
	v_lshl_add_u64 v[218:219], s[30:31], 0, v[136:137]
	ds_read_b128 v[184:187], v151 offset:16384
	ds_read_b128 v[188:191], v151 offset:17408
	ds_read_b128 v[192:195], v151 offset:18432
	ds_read_b128 v[196:199], v151 offset:19456
	ds_read_b128 v[202:205], v151 offset:20480
	ds_read_b128 v[206:209], v151 offset:21504
	ds_read_b128 v[210:213], v151 offset:22528
	ds_read_b128 v[214:217], v151 offset:23552
	global_load_lds_dwordx4 v[218:219], off
	s_mov_b32 m0, s59
	s_cselect_b32 s59, 0, s29
	s_cselect_b32 s61, 0, s28
	s_cselect_b32 s62, s11, s15
	s_cselect_b32 s63, s10, s14
	s_add_u32 s34, s30, 0x160000
	v_lshl_add_u64 v[220:221], s[30:31], 0, v[140:141]
	s_addc_u32 s35, s31, 0
	s_add_i32 s60, s60, s33
	global_load_lds_dwordx4 v[220:221], off
	v_lshl_add_u64 v[222:223], s[34:35], 0, v[136:137]
	s_mov_b32 m0, s60
	s_nop 0
	global_load_lds_dwordx4 v[222:223], off
	s_add_i32 m0, s60, 0x2000
	v_lshl_add_u64 v[222:223], s[34:35], 0, v[140:141]
	s_add_u32 s34, s63, s61
	s_addc_u32 s35, s62, s59
	global_load_lds_dwordx4 v[222:223], off
	v_lshl_add_u64 v[222:223], s[34:35], 0, v[134:135]
	s_mov_b32 m0, s44
	v_lshl_add_u64 v[224:225], s[34:35], 0, v[138:139]
	global_load_lds_dwordx4 v[222:223], off
	s_mov_b32 m0, s45
	s_nop 0
	global_load_lds_dwordx4 v[224:225], off
	s_waitcnt vmcnt(8)
	s_waitcnt lgkmcnt(0)
	s_barrier
; #define PG8_STAGE_A(bufoff, base_, nx_, kb_, h_) do { if (GATHER) { if (nx_) PG8_STAGE_G(bufoff, kb_, goN, h_); else PG8_STAGE_G(bufoff, kb_, goC, h_); } \
;         else PG8_STAGE(bufoff, (base_) + (kb_) + (h_) * hstep, voffA); } while (0)
; #define PG8_LDA(dst, b, h) do { _Pragma("unroll") for (int m = 0; m < 4; ++m) _Pragma("unroll") for (int k = 0; k < 2; ++k) dst[m][k] = *(const LAS bf16x8*)(lds + PG8_SA(b, h) + aoff + m * 2048 + k * 1024); } while (0)
; #define PG8_LDB(dst, b, h) do { _Pragma("unroll") for (int n = 0; n < 2; ++n) _Pragma("unroll") for (int k = 0; k < 2; ++k) dst[n][k] = *(const LAS bf16x8*)(lds + PG8_SB(b, h) + boff + n * 2048 + k * 1024); } while (0)
; #define PG8_MMA(ai, bj, At, Bt) do { __builtin_amdgcn_s_setprio(1); _Pragma("unroll") for (int m = 0; m < 4; ++m) _Pragma("unroll") for (int n = 0; n < 2; ++n) _Pragma("unroll") for (int k = 0; k < 2; ++k) \
;         acc[ai][bj][m][n] = __builtin_amdgcn_mfma_f32_16x16x32_bf16(Bt[n][k], At[m][k], acc[ai][bj][m][n], 0, 0, 0); __builtin_amdgcn_s_setprio(0); } while (0)
; #define PG8_WAIT_V(n) asm volatile("s_waitcnt vmcnt(" #n ")" ::: "memory")
; #define PG8_WAIT_L(n) asm volatile("s_waitcnt lgkmcnt(" #n ")" ::: "memory")
; #define PG8_BAR __builtin_amdgcn_s_barrier()
; #define PG8_SCHED __builtin_amdgcn_sched_barrier(0)
; template <class Epi, class Sched, bool GATHER = false>
; __device__ __forceinline__ void gemm_phase(LAS unsigned char* lds, const Gemm g, const Sched& S, const Epi& E, const int tid) {
;     ...
;             PG8_WAIT_V(8); PG8_WAIT_L(0); PG8_BAR; PG8_MMA(1, 0, At, B0); PG8_MMA(1, 1, At, B1); PG8_BAR; PG8_SCHED;
;             PG8_LDB(B0, 1, 0); PG8_LDB(B1, 1, 1); PG8_SCHED; PG8_LDA(At, 1, 0); PG8_STAGE_A(PG8_SA(0, 1), (last ? nA : cA), last, kb2, 1);
;             PG8_WAIT_V(8); PG8_WAIT_L(0); PG8_BAR; PG8_MMA(0, 0, At, B0); PG8_MMA(0, 1, At, B1); PG8_BAR; PG8_SCHED;
	s_waitcnt lgkmcnt(0)
	v_mfma_f32_16x16x32_bf16 v[58:61], v[152:155], v[184:187], v[58:61]
	v_mfma_f32_16x16x32_bf16 v[78:81], v[160:163], v[184:187], v[78:81]
	v_mfma_f32_16x16x32_bf16 v[66:69], v[152:155], v[192:195], v[66:69]
	v_mfma_f32_16x16x32_bf16 v[82:85], v[160:163], v[192:195], v[82:85]
	v_mfma_f32_16x16x32_bf16 v[74:77], v[152:155], v[202:205], v[74:77]
	v_mfma_f32_16x16x32_bf16 v[98:101], v[160:163], v[202:205], v[98:101]
	v_mfma_f32_16x16x32_bf16 v[90:93], v[152:155], v[210:213], v[90:93]
	v_mfma_f32_16x16x32_bf16 v[94:97], v[160:163], v[210:213], v[94:97]
	v_mfma_f32_16x16x32_bf16 v[58:61], v[156:159], v[188:191], v[58:61]
	v_mfma_f32_16x16x32_bf16 v[78:81], v[164:167], v[188:191], v[78:81]
	v_mfma_f32_16x16x32_bf16 v[66:69], v[156:159], v[196:199], v[66:69]
	v_mfma_f32_16x16x32_bf16 v[82:85], v[164:167], v[196:199], v[82:85]
	v_mfma_f32_16x16x32_bf16 v[74:77], v[156:159], v[206:209], v[74:77]
	v_mfma_f32_16x16x32_bf16 v[98:101], v[164:167], v[206:209], v[98:101]
	v_mfma_f32_16x16x32_bf16 v[90:93], v[156:159], v[214:217], v[90:93]
	v_mfma_f32_16x16x32_bf16 v[94:97], v[164:167], v[214:217], v[94:97]
	v_mfma_f32_16x16x32_bf16 v[114:117], v[168:171], v[184:187], v[114:117]
	v_mfma_f32_16x16x32_bf16 v[130:133], v[176:179], v[184:187], v[130:133]
	v_mfma_f32_16x16x32_bf16 v[110:113], v[168:171], v[192:195], v[110:113]
	v_mfma_f32_16x16x32_bf16 v[126:129], v[176:179], v[192:195], v[126:129]
	v_mfma_f32_16x16x32_bf16 v[106:109], v[168:171], v[202:205], v[106:109]
	v_mfma_f32_16x16x32_bf16 v[122:125], v[176:179], v[202:205], v[122:125]
	v_mfma_f32_16x16x32_bf16 v[102:105], v[168:171], v[210:213], v[102:105]
	v_mfma_f32_16x16x32_bf16 v[118:121], v[176:179], v[210:213], v[118:121]
	v_mfma_f32_16x16x32_bf16 v[114:117], v[172:175], v[188:191], v[114:117]
	v_mfma_f32_16x16x32_bf16 v[130:133], v[180:183], v[188:191], v[130:133]
	v_mfma_f32_16x16x32_bf16 v[110:113], v[172:175], v[196:199], v[110:113]
	v_mfma_f32_16x16x32_bf16 v[126:129], v[180:183], v[196:199], v[126:129]
	v_mfma_f32_16x16x32_bf16 v[106:109], v[172:175], v[206:209], v[106:109]
	v_mfma_f32_16x16x32_bf16 v[122:125], v[180:183], v[206:209], v[122:125]
	v_mfma_f32_16x16x32_bf16 v[102:105], v[172:175], v[214:217], v[102:105]
	v_mfma_f32_16x16x32_bf16 v[118:121], v[180:183], v[214:217], v[118:121]
	s_barrier
	s_add_i32 s59, 0, 0x18000
	v_add_u32_e32 v2, s59, v149
	s_add_i32 s60, 0, 0x1c000
	ds_read_b128 v[152:155], v2
	ds_read_b128 v[156:159], v2 offset:1024
	ds_read_b128 v[160:163], v2 offset:2048
	ds_read_b128 v[164:167], v2 offset:3072
	v_add_u32_e32 v2, s60, v149
	ds_read_b128 v[168:171], v2
	ds_read_b128 v[172:175], v2 offset:1024
	ds_read_b128 v[176:179], v2 offset:2048
	ds_read_b128 v[180:183], v2 offset:3072
	s_add_u32 s34, s34, 0x160000
	s_addc_u32 s35, s35, 0
	s_mov_b32 m0, s46
	v_lshl_add_u64 v[226:227], s[34:35], 0, v[134:135]
	ds_read_b128 v[184:187], v151 offset:32768
	ds_read_b128 v[188:191], v151 offset:33792
	ds_read_b128 v[192:195], v151 offset:34816
	ds_read_b128 v[196:199], v151 offset:35840
	ds_read_b128 v[202:205], v151 offset:36864
	ds_read_b128 v[206:209], v151 offset:37888
	ds_read_b128 v[210:213], v151 offset:38912
	ds_read_b128 v[214:217], v151 offset:39936
	global_load_lds_dwordx4 v[226:227], off
	v_lshl_add_u64 v[226:227], s[34:35], 0, v[138:139]
	s_mov_b32 m0, s47
	s_nop 0
	global_load_lds_dwordx4 v[226:227], off
	s_waitcnt vmcnt(8)
	s_waitcnt lgkmcnt(0)
	s_barrier
	s_waitcnt lgkmcnt(0)
	v_mfma_f32_16x16x32_bf16 v[86:89], v[152:155], v[184:187], v[86:89]
	v_mfma_f32_16x16x32_bf16 v[18:21], v[160:163], v[184:187], v[18:21]
	v_mfma_f32_16x16x32_bf16 v[6:9], v[152:155], v[192:195], v[6:9]
	v_mfma_f32_16x16x32_bf16 v[22:25], v[160:163], v[192:195], v[22:25]
	v_mfma_f32_16x16x32_bf16 v[10:13], v[152:155], v[202:205], v[10:13]
	v_mfma_f32_16x16x32_bf16 v[26:29], v[160:163], v[202:205], v[26:29]
	v_mfma_f32_16x16x32_bf16 v[14:17], v[152:155], v[210:213], v[14:17]
	v_mfma_f32_16x16x32_bf16 v[30:33], v[160:163], v[210:213], v[30:33]
	v_mfma_f32_16x16x32_bf16 v[86:89], v[156:159], v[188:191], v[86:89]
	v_mfma_f32_16x16x32_bf16 v[18:21], v[164:167], v[188:191], v[18:21]
	v_mfma_f32_16x16x32_bf16 v[6:9], v[156:159], v[196:199], v[6:9]
	v_mfma_f32_16x16x32_bf16 v[22:25], v[164:167], v[196:199], v[22:25]
	v_mfma_f32_16x16x32_bf16 v[10:13], v[156:159], v[206:209], v[10:13]
	v_mfma_f32_16x16x32_bf16 v[26:29], v[164:167], v[206:209], v[26:29]
	v_mfma_f32_16x16x32_bf16 v[14:17], v[156:159], v[214:217], v[14:17]
	v_mfma_f32_16x16x32_bf16 v[30:33], v[164:167], v[214:217], v[30:33]
	v_mfma_f32_16x16x32_bf16 v[34:37], v[168:171], v[184:187], v[34:37]
	v_mfma_f32_16x16x32_bf16 v[50:53], v[176:179], v[184:187], v[50:53]
	v_mfma_f32_16x16x32_bf16 v[38:41], v[168:171], v[192:195], v[38:41]
	v_mfma_f32_16x16x32_bf16 v[54:57], v[176:179], v[192:195], v[54:57]
	v_mfma_f32_16x16x32_bf16 v[42:45], v[168:171], v[202:205], v[42:45]
	v_mfma_f32_16x16x32_bf16 v[62:65], v[176:179], v[202:205], v[62:65]
	v_mfma_f32_16x16x32_bf16 v[46:49], v[168:171], v[210:213], v[46:49]
	v_mfma_f32_16x16x32_bf16 v[70:73], v[176:179], v[210:213], v[70:73]
	v_mfma_f32_16x16x32_bf16 v[34:37], v[172:175], v[188:191], v[34:37]
	v_mfma_f32_16x16x32_bf16 v[50:53], v[180:183], v[188:191], v[50:53]
	v_mfma_f32_16x16x32_bf16 v[38:41], v[172:175], v[196:199], v[38:41]
	v_mfma_f32_16x16x32_bf16 v[54:57], v[180:183], v[196:199], v[54:57]
	v_mfma_f32_16x16x32_bf16 v[42:45], v[172:175], v[206:209], v[42:45]
	v_mfma_f32_16x16x32_bf16 v[62:65], v[180:183], v[206:209], v[62:65]
	v_mfma_f32_16x16x32_bf16 v[46:49], v[172:175], v[214:217], v[46:49]
	v_mfma_f32_16x16x32_bf16 v[70:73], v[180:183], v[214:217], v[70:73]
	s_barrier
; #define PG8_STAGE_A(bufoff, base_, nx_, kb_, h_) do { if (GATHER) { if (nx_) PG8_STAGE_G(bufoff, kb_, goN, h_); else PG8_STAGE_G(bufoff, kb_, goC, h_); } \
;         else PG8_STAGE(bufoff, (base_) + (kb_) + (h_) * hstep, voffA); } while (0)
; #define PG8_STAGE(bufoff, gbase, voff) do { _Pragma("unroll") for (int _i = 0; _i < 2; ++_i) \
;         __builtin_amdgcn_global_load_lds((const unsigned*)((const char*)(gbase) + (voff)[_i]), (LAS unsigned*)(lds + (bufoff) + ldsw + _i * 8192), 16, 0, 0); } while (0)
; #define PG8_LDA(dst, b, h) do { _Pragma("unroll") for (int m = 0; m < 4; ++m) _Pragma("unroll") for (int k = 0; k < 2; ++k) dst[m][k] = *(const LAS bf16x8*)(lds + PG8_SA(b, h) + aoff + m * 2048 + k * 1024); } while (0)
; #define PG8_MMA(ai, bj, At, Bt) do { __builtin_amdgcn_s_setprio(1); _Pragma("unroll") for (int m = 0; m < 4; ++m) _Pragma("unroll") for (int n = 0; n < 2; ++n) _Pragma("unroll") for (int k = 0; k < 2; ++k) \
;         acc[ai][bj][m][n] = __builtin_amdgcn_mfma_f32_16x16x32_bf16(Bt[n][k], At[m][k], acc[ai][bj][m][n], 0, 0, 0); __builtin_amdgcn_s_setprio(0); } while (0)
; #define PG8_WAIT_V(n) asm volatile("s_waitcnt vmcnt(" #n ")" ::: "memory")
; #define PG8_WAIT_L(n) asm volatile("s_waitcnt lgkmcnt(" #n ")" ::: "memory")
; #define PG8_BAR __builtin_amdgcn_s_barrier()
; #define PG8_SCHED __builtin_amdgcn_sched_barrier(0)
; template <class Epi, class Sched, bool GATHER = false>
; __device__ __forceinline__ void gemm_phase(LAS unsigned char* lds, const Gemm g, const Sched& S, const Epi& E, const int tid) {
;     ...
;             PG8_LDA(At, 1, 1); PG8_STAGE(PG8_SB(1, 0), b3, voffB); PG8_STAGE(PG8_SB(1, 1), b3 + hstep, voffB); PG8_STAGE_A(PG8_SA(1, 0), (last ? nA : cA), last, kb3, 0);
;             PG8_WAIT_V(8); PG8_WAIT_L(0); PG8_BAR; PG8_MMA(1, 0, At, B0); PG8_MMA(1, 1, At, B1); PG8_BAR; PG8_SCHED;
	s_add_i32 s34, s59, s33
	v_lshl_add_u64 v[218:219], v[218:219], 0, s[0:1]
	s_mov_b32 m0, s34
	ds_read_b128 v[184:187], v151 offset:49152
	ds_read_b128 v[188:191], v151 offset:50176
	ds_read_b128 v[192:195], v151 offset:51200
	ds_read_b128 v[196:199], v151 offset:52224
	ds_read_b128 v[202:205], v151 offset:53248
	ds_read_b128 v[206:209], v151 offset:54272
	ds_read_b128 v[210:213], v151 offset:55296
	ds_read_b128 v[214:217], v151 offset:56320
	global_load_lds_dwordx4 v[218:219], off
	s_add_i32 m0, s34, 0x2000
	s_add_u32 s30, s30, 0x160080
	v_lshl_add_u64 v[218:219], v[220:221], 0, s[0:1]
	s_addc_u32 s31, s31, 0
	s_add_i32 s34, s60, s33
	global_load_lds_dwordx4 v[218:219], off
	v_lshl_add_u64 v[218:219], s[30:31], 0, v[136:137]
	s_mov_b32 m0, s34
	s_nop 0
	global_load_lds_dwordx4 v[218:219], off
	v_lshl_add_u64 v[218:219], s[30:31], 0, v[140:141]
	s_add_i32 m0, s34, 0x2000
	s_nop 0
	global_load_lds_dwordx4 v[218:219], off
	v_lshl_add_u64 v[218:219], v[222:223], 0, s[0:1]
	s_mov_b32 m0, s48
	s_nop 0
	global_load_lds_dwordx4 v[218:219], off
	v_lshl_add_u64 v[218:219], v[224:225], 0, s[0:1]
	s_mov_b32 m0, s49
	s_nop 0
	global_load_lds_dwordx4 v[218:219], off
	s_waitcnt vmcnt(8)
	s_waitcnt lgkmcnt(0)
	s_barrier
	s_waitcnt lgkmcnt(0)
	v_mfma_f32_16x16x32_bf16 v[58:61], v[152:155], v[184:187], v[58:61]
	v_mfma_f32_16x16x32_bf16 v[78:81], v[160:163], v[184:187], v[78:81]
	v_mfma_f32_16x16x32_bf16 v[66:69], v[152:155], v[192:195], v[66:69]
	v_mfma_f32_16x16x32_bf16 v[82:85], v[160:163], v[192:195], v[82:85]
	v_mfma_f32_16x16x32_bf16 v[74:77], v[152:155], v[202:205], v[74:77]
	v_mfma_f32_16x16x32_bf16 v[98:101], v[160:163], v[202:205], v[98:101]
	v_mfma_f32_16x16x32_bf16 v[90:93], v[152:155], v[210:213], v[90:93]
	v_mfma_f32_16x16x32_bf16 v[94:97], v[160:163], v[210:213], v[94:97]
	v_mfma_f32_16x16x32_bf16 v[58:61], v[156:159], v[188:191], v[58:61]
	v_mfma_f32_16x16x32_bf16 v[78:81], v[164:167], v[188:191], v[78:81]
	v_mfma_f32_16x16x32_bf16 v[66:69], v[156:159], v[196:199], v[66:69]
	v_mfma_f32_16x16x32_bf16 v[82:85], v[164:167], v[196:199], v[82:85]
	v_mfma_f32_16x16x32_bf16 v[74:77], v[156:159], v[206:209], v[74:77]
	v_mfma_f32_16x16x32_bf16 v[98:101], v[164:167], v[206:209], v[98:101]
	v_mfma_f32_16x16x32_bf16 v[90:93], v[156:159], v[214:217], v[90:93]
	v_mfma_f32_16x16x32_bf16 v[94:97], v[164:167], v[214:217], v[94:97]
	v_mfma_f32_16x16x32_bf16 v[114:117], v[168:171], v[184:187], v[114:117]
	v_mfma_f32_16x16x32_bf16 v[130:133], v[176:179], v[184:187], v[130:133]
	v_mfma_f32_16x16x32_bf16 v[110:113], v[168:171], v[192:195], v[110:113]
	v_mfma_f32_16x16x32_bf16 v[126:129], v[176:179], v[192:195], v[126:129]
	v_mfma_f32_16x16x32_bf16 v[106:109], v[168:171], v[202:205], v[106:109]
	v_mfma_f32_16x16x32_bf16 v[122:125], v[176:179], v[202:205], v[122:125]
	v_mfma_f32_16x16x32_bf16 v[102:105], v[168:171], v[210:213], v[102:105]
	v_mfma_f32_16x16x32_bf16 v[118:121], v[176:179], v[210:213], v[118:121]
	v_mfma_f32_16x16x32_bf16 v[114:117], v[172:175], v[188:191], v[114:117]
	v_mfma_f32_16x16x32_bf16 v[130:133], v[180:183], v[188:191], v[130:133]
	v_mfma_f32_16x16x32_bf16 v[110:113], v[172:175], v[196:199], v[110:113]
	v_mfma_f32_16x16x32_bf16 v[126:129], v[180:183], v[196:199], v[126:129]
	v_mfma_f32_16x16x32_bf16 v[106:109], v[172:175], v[206:209], v[106:109]
	v_mfma_f32_16x16x32_bf16 v[122:125], v[180:183], v[206:209], v[122:125]
	v_mfma_f32_16x16x32_bf16 v[102:105], v[172:175], v[214:217], v[102:105]
	v_mfma_f32_16x16x32_bf16 v[118:121], v[180:183], v[214:217], v[118:121]
	s_barrier
	s_add_i32 s58, s58, 2
	s_cmpk_gt_u32 s58, 0x55
	s_mov_b64 s[34:35], s[28:29]
	s_cbranch_scc0 .LBB0_1483
	s_and_b64 vcc, exec, s[16:17]
	s_cbranch_vccz .LBB0_1486
	s_barrier

; #define PG8_STAGE_A(bufoff, base_, nx_, kb_, h_) do { if (GATHER) { if (nx_) PG8_STAGE_G(bufoff, kb_, goN, h_); else PG8_STAGE_G(bufoff, kb_, goC, h_); } \
;         else PG8_STAGE(bufoff, (base_) + (kb_) + (h_) * hstep, voffA); } while (0)
; #define PG8_STAGE(bufoff, gbase, voff) do { _Pragma("unroll") for (int _i = 0; _i < 2; ++_i) \
;         __builtin_amdgcn_global_load_lds((const unsigned*)((const char*)(gbase) + (voff)[_i]), (LAS unsigned*)(lds + (bufoff) + ldsw + _i * 8192), 16, 0, 0); } while (0)
; #define PG8_LDA(dst, b, h) do { _Pragma("unroll") for (int m = 0; m < 4; ++m) _Pragma("unroll") for (int k = 0; k < 2; ++k) dst[m][k] = *(const LAS bf16x8*)(lds + PG8_SA(b, h) + aoff + m * 2048 + k * 1024); } while (0)
; #define PG8_LDB(dst, b, h) do { _Pragma("unroll") for (int n = 0; n < 2; ++n) _Pragma("unroll") for (int k = 0; k < 2; ++k) dst[n][k] = *(const LAS bf16x8*)(lds + PG8_SB(b, h) + boff + n * 2048 + k * 1024); } while (0)
; #define PG8_MMA(ai, bj, At, Bt) do { __builtin_amdgcn_s_setprio(1); _Pragma("unroll") for (int m = 0; m < 4; ++m) _Pragma("unroll") for (int n = 0; n < 2; ++n) _Pragma("unroll") for (int k = 0; k < 2; ++k) \
;         acc[ai][bj][m][n] = __builtin_amdgcn_mfma_f32_16x16x32_bf16(Bt[n][k], At[m][k], acc[ai][bj][m][n], 0, 0, 0); __builtin_amdgcn_s_setprio(0); } while (0)
; #define PG8_WAIT_V(n) asm volatile("s_waitcnt vmcnt(" #n ")" ::: "memory")
; #define PG8_WAIT_L(n) asm volatile("s_waitcnt lgkmcnt(" #n ")" ::: "memory")
; #define PG8_BAR __builtin_amdgcn_s_barrier()
; #define PG8_SCHED __builtin_amdgcn_sched_barrier(0)
; template <class Epi, class Sched, bool GATHER = false>
; __device__ __forceinline__ void gemm_phase(LAS unsigned char* lds, const Gemm g, const Sched& S, const Epi& E, const int tid) {
;     ...
;             PG8_LDB(B0, 0, 0); PG8_LDB(B1, 0, 1); PG8_SCHED; PG8_LDA(At, 0, 0); PG8_STAGE_A(PG8_SA(1, 1), cA, false, kb1, 1);
;             PG8_WAIT_V(8); PG8_WAIT_L(0); PG8_BAR; PG8_MMA(0, 0, At, B0); PG8_MMA(0, 1, At, B1); PG8_BAR; PG8_SCHED;
;             PG8_LDA(At, 0, 1); PG8_STAGE(PG8_SB(0, 0), b2, voffB); PG8_STAGE(PG8_SB(0, 1), b2 + hstep, voffB); PG8_STAGE_A(PG8_SA(0, 0), (last ? nA : cA), last, kb2, 0);
;             PG8_WAIT_V(8); PG8_WAIT_L(0); PG8_BAR; PG8_MMA(1, 0, At, B0); PG8_MMA(1, 1, At, B1); PG8_BAR; PG8_SCHED;
.LBB0_1505:
	s_add_u32 s30, s34, 0x100
	s_addc_u32 s31, s35, 0
	s_add_i32 s64, 0, 0x10000
	s_add_i32 s65, 0, 0x14000
	v_add_u32_e32 v2, s64, v153
	ds_read_b128 v[158:161], v2
	ds_read_b128 v[162:165], v2 offset:1024
	ds_read_b128 v[166:169], v2 offset:2048
	ds_read_b128 v[170:173], v2 offset:3072
	v_add_u32_e32 v2, s65, v153
	ds_read_b128 v[174:177], v2
	ds_read_b128 v[178:181], v2 offset:1024
	ds_read_b128 v[182:185], v2 offset:2048
	ds_read_b128 v[186:189], v2 offset:3072
	s_add_i32 s67, s64, s48
	s_add_i32 m0, s51, 0xc000
	s_add_i32 s66, s51, 0xe000
	s_add_i32 s68, s67, 0x2000
	s_cmp_eq_u32 s63, 40
	v_lshl_add_u64 v[190:191], v[4:5], 0, s[34:35]
	s_cselect_b64 vcc, -1, 0
	v_cndmask_b32_e32 v199, v191, v147, vcc
	v_cndmask_b32_e32 v198, v190, v146, vcc
	s_cselect_b32 s64, 0, s30
	v_lshl_add_u64 v[226:227], v[148:149], 0, s[34:35]
	ds_read_b128 v[190:193], v155
	ds_read_b128 v[194:197], v155 offset:1024
	ds_read_b128 v[202:205], v155 offset:2048
	ds_read_b128 v[206:209], v155 offset:3072
	ds_read_b128 v[210:213], v155 offset:4096
	ds_read_b128 v[214:217], v155 offset:5120
	ds_read_b128 v[218:221], v155 offset:6144
	ds_read_b128 v[222:225], v155 offset:7168
	global_load_lds_dwordx4 v[226:227], off
	v_lshl_add_u64 v[226:227], v[150:151], 0, s[34:35]
	s_mov_b32 m0, s66
	s_nop 0
	global_load_lds_dwordx4 v[226:227], off
	s_waitcnt vmcnt(8)
	s_waitcnt lgkmcnt(0)
	s_barrier
	s_waitcnt lgkmcnt(0)
	v_mfma_f32_16x16x32_bf16 v[90:93], v[158:161], v[190:193], v[90:93]
	v_mfma_f32_16x16x32_bf16 v[18:21], v[166:169], v[190:193], v[18:21]
	v_mfma_f32_16x16x32_bf16 v[6:9], v[158:161], v[202:205], v[6:9]
	v_mfma_f32_16x16x32_bf16 v[22:25], v[166:169], v[202:205], v[22:25]
	v_mfma_f32_16x16x32_bf16 v[10:13], v[158:161], v[210:213], v[10:13]
	v_mfma_f32_16x16x32_bf16 v[26:29], v[166:169], v[210:213], v[26:29]
	v_mfma_f32_16x16x32_bf16 v[14:17], v[158:161], v[218:221], v[14:17]
	v_mfma_f32_16x16x32_bf16 v[30:33], v[166:169], v[218:221], v[30:33]
	v_mfma_f32_16x16x32_bf16 v[90:93], v[162:165], v[194:197], v[90:93]
	v_mfma_f32_16x16x32_bf16 v[18:21], v[170:173], v[194:197], v[18:21]
	v_mfma_f32_16x16x32_bf16 v[6:9], v[162:165], v[206:209], v[6:9]
	v_mfma_f32_16x16x32_bf16 v[22:25], v[170:173], v[206:209], v[22:25]
	v_mfma_f32_16x16x32_bf16 v[10:13], v[162:165], v[214:217], v[10:13]
	v_mfma_f32_16x16x32_bf16 v[26:29], v[170:173], v[214:217], v[26:29]
	v_mfma_f32_16x16x32_bf16 v[14:17], v[162:165], v[222:225], v[14:17]
	v_mfma_f32_16x16x32_bf16 v[30:33], v[170:173], v[222:225], v[30:33]
	v_mfma_f32_16x16x32_bf16 v[34:37], v[174:177], v[190:193], v[34:37]
	v_mfma_f32_16x16x32_bf16 v[50:53], v[182:185], v[190:193], v[50:53]
	v_mfma_f32_16x16x32_bf16 v[38:41], v[174:177], v[202:205], v[38:41]
	v_mfma_f32_16x16x32_bf16 v[54:57], v[182:185], v[202:205], v[54:57]
	v_mfma_f32_16x16x32_bf16 v[42:45], v[174:177], v[210:213], v[42:45]
	v_mfma_f32_16x16x32_bf16 v[62:65], v[182:185], v[210:213], v[62:65]
	v_mfma_f32_16x16x32_bf16 v[46:49], v[174:177], v[218:221], v[46:49]
	v_mfma_f32_16x16x32_bf16 v[70:73], v[182:185], v[218:221], v[70:73]
	v_mfma_f32_16x16x32_bf16 v[34:37], v[178:181], v[194:197], v[34:37]
	v_mfma_f32_16x16x32_bf16 v[50:53], v[186:189], v[194:197], v[50:53]
	v_mfma_f32_16x16x32_bf16 v[38:41], v[178:181], v[206:209], v[38:41]
	v_mfma_f32_16x16x32_bf16 v[54:57], v[186:189], v[206:209], v[54:57]
	v_mfma_f32_16x16x32_bf16 v[42:45], v[178:181], v[214:217], v[42:45]
	v_mfma_f32_16x16x32_bf16 v[62:65], v[186:189], v[214:217], v[62:65]
	v_mfma_f32_16x16x32_bf16 v[46:49], v[178:181], v[222:225], v[46:49]
	v_mfma_f32_16x16x32_bf16 v[70:73], v[186:189], v[222:225], v[70:73]
	s_barrier
	s_mov_b32 m0, s67
	v_lshl_add_u64 v[226:227], v[198:199], 0, v[138:139]
	ds_read_b128 v[190:193], v155 offset:16384
	ds_read_b128 v[194:197], v155 offset:17408
	ds_read_b128 v[202:205], v155 offset:18432
	ds_read_b128 v[206:209], v155 offset:19456
	ds_read_b128 v[210:213], v155 offset:20480
	ds_read_b128 v[214:217], v155 offset:21504
	ds_read_b128 v[218:221], v155 offset:22528
	ds_read_b128 v[222:225], v155 offset:23552
	global_load_lds_dwordx4 v[226:227], off
	v_lshl_add_u64 v[228:229], v[198:199], 0, v[134:135]
	s_mov_b32 m0, s68
	s_cselect_b32 s35, s11, s29
	s_cselect_b32 s34, s10, s28
	v_lshl_add_u64 v[230:231], v[198:199], 0, s[72:73]
	s_add_i32 s65, s65, s48
	global_load_lds_dwordx4 v[228:229], off
	v_lshl_add_u64 v[232:233], v[230:231], 0, v[138:139]
	s_mov_b32 m0, s65
	v_lshl_add_u64 v[230:231], v[230:231], 0, v[134:135]
	global_load_lds_dwordx4 v[232:233], off
	s_add_i32 m0, s65, 0x2000
	s_add_u32 s34, s34, s64
	s_addc_u32 s35, s35, 0
	global_load_lds_dwordx4 v[230:231], off
	v_lshl_add_u64 v[230:231], s[34:35], 0, v[140:141]
	s_mov_b32 m0, s51
	v_lshl_add_u64 v[232:233], s[34:35], 0, v[136:137]
	global_load_lds_dwordx4 v[230:231], off
	s_mov_b32 m0, s52
	s_nop 0
	global_load_lds_dwordx4 v[232:233], off
	s_waitcnt vmcnt(8)
	s_waitcnt lgkmcnt(0)
	s_barrier
; #define PG8_STAGE_A(bufoff, base_, nx_, kb_, h_) do { if (GATHER) { if (nx_) PG8_STAGE_G(bufoff, kb_, goN, h_); else PG8_STAGE_G(bufoff, kb_, goC, h_); } \
;         else PG8_STAGE(bufoff, (base_) + (kb_) + (h_) * hstep, voffA); } while (0)
; #define PG8_LDA(dst, b, h) do { _Pragma("unroll") for (int m = 0; m < 4; ++m) _Pragma("unroll") for (int k = 0; k < 2; ++k) dst[m][k] = *(const LAS bf16x8*)(lds + PG8_SA(b, h) + aoff + m * 2048 + k * 1024); } while (0)
; #define PG8_LDB(dst, b, h) do { _Pragma("unroll") for (int n = 0; n < 2; ++n) _Pragma("unroll") for (int k = 0; k < 2; ++k) dst[n][k] = *(const LAS bf16x8*)(lds + PG8_SB(b, h) + boff + n * 2048 + k * 1024); } while (0)
; #define PG8_MMA(ai, bj, At, Bt) do { __builtin_amdgcn_s_setprio(1); _Pragma("unroll") for (int m = 0; m < 4; ++m) _Pragma("unroll") for (int n = 0; n < 2; ++n) _Pragma("unroll") for (int k = 0; k < 2; ++k) \
;         acc[ai][bj][m][n] = __builtin_amdgcn_mfma_f32_16x16x32_bf16(Bt[n][k], At[m][k], acc[ai][bj][m][n], 0, 0, 0); __builtin_amdgcn_s_setprio(0); } while (0)
; #define PG8_WAIT_V(n) asm volatile("s_waitcnt vmcnt(" #n ")" ::: "memory")
; #define PG8_WAIT_L(n) asm volatile("s_waitcnt lgkmcnt(" #n ")" ::: "memory")
; #define PG8_BAR __builtin_amdgcn_s_barrier()
; #define PG8_SCHED __builtin_amdgcn_sched_barrier(0)
; template <class Epi, class Sched, bool GATHER = false>
; __device__ __forceinline__ void gemm_phase(LAS unsigned char* lds, const Gemm g, const Sched& S, const Epi& E, const int tid) {
;     ...
;             PG8_WAIT_V(8); PG8_WAIT_L(0); PG8_BAR; PG8_MMA(1, 0, At, B0); PG8_MMA(1, 1, At, B1); PG8_BAR; PG8_SCHED;
;             PG8_LDB(B0, 1, 0); PG8_LDB(B1, 1, 1); PG8_SCHED; PG8_LDA(At, 1, 0); PG8_STAGE_A(PG8_SA(0, 1), (last ? nA : cA), last, kb2, 1);
;             PG8_WAIT_V(8); PG8_WAIT_L(0); PG8_BAR; PG8_MMA(0, 0, At, B0); PG8_MMA(0, 1, At, B1); PG8_BAR; PG8_SCHED;
	s_waitcnt lgkmcnt(0)
	v_mfma_f32_16x16x32_bf16 v[58:61], v[158:161], v[190:193], v[58:61]
	v_mfma_f32_16x16x32_bf16 v[78:81], v[166:169], v[190:193], v[78:81]
	v_mfma_f32_16x16x32_bf16 v[66:69], v[158:161], v[202:205], v[66:69]
	v_mfma_f32_16x16x32_bf16 v[82:85], v[166:169], v[202:205], v[82:85]
	v_mfma_f32_16x16x32_bf16 v[74:77], v[158:161], v[210:213], v[74:77]
	v_mfma_f32_16x16x32_bf16 v[86:89], v[166:169], v[210:213], v[86:89]
	v_mfma_f32_16x16x32_bf16 v[94:97], v[158:161], v[218:221], v[94:97]
	v_mfma_f32_16x16x32_bf16 v[98:101], v[166:169], v[218:221], v[98:101]
	v_mfma_f32_16x16x32_bf16 v[58:61], v[162:165], v[194:197], v[58:61]
	v_mfma_f32_16x16x32_bf16 v[78:81], v[170:173], v[194:197], v[78:81]
	v_mfma_f32_16x16x32_bf16 v[66:69], v[162:165], v[206:209], v[66:69]
	v_mfma_f32_16x16x32_bf16 v[82:85], v[170:173], v[206:209], v[82:85]
	v_mfma_f32_16x16x32_bf16 v[74:77], v[162:165], v[214:217], v[74:77]
	v_mfma_f32_16x16x32_bf16 v[86:89], v[170:173], v[214:217], v[86:89]
	v_mfma_f32_16x16x32_bf16 v[94:97], v[162:165], v[222:225], v[94:97]
	v_mfma_f32_16x16x32_bf16 v[98:101], v[170:173], v[222:225], v[98:101]
	v_mfma_f32_16x16x32_bf16 v[114:117], v[174:177], v[190:193], v[114:117]
	v_mfma_f32_16x16x32_bf16 v[130:133], v[182:185], v[190:193], v[130:133]
	v_mfma_f32_16x16x32_bf16 v[110:113], v[174:177], v[202:205], v[110:113]
	v_mfma_f32_16x16x32_bf16 v[126:129], v[182:185], v[202:205], v[126:129]
	v_mfma_f32_16x16x32_bf16 v[106:109], v[174:177], v[210:213], v[106:109]
	v_mfma_f32_16x16x32_bf16 v[122:125], v[182:185], v[210:213], v[122:125]
	v_mfma_f32_16x16x32_bf16 v[102:105], v[174:177], v[218:221], v[102:105]
	v_mfma_f32_16x16x32_bf16 v[118:121], v[182:185], v[218:221], v[118:121]
	v_mfma_f32_16x16x32_bf16 v[114:117], v[178:181], v[194:197], v[114:117]
	v_mfma_f32_16x16x32_bf16 v[130:133], v[186:189], v[194:197], v[130:133]
	v_mfma_f32_16x16x32_bf16 v[110:113], v[178:181], v[206:209], v[110:113]
	v_mfma_f32_16x16x32_bf16 v[126:129], v[186:189], v[206:209], v[126:129]
	v_mfma_f32_16x16x32_bf16 v[106:109], v[178:181], v[214:217], v[106:109]
	v_mfma_f32_16x16x32_bf16 v[122:125], v[186:189], v[214:217], v[122:125]
	v_mfma_f32_16x16x32_bf16 v[102:105], v[178:181], v[222:225], v[102:105]
	v_mfma_f32_16x16x32_bf16 v[118:121], v[186:189], v[222:225], v[118:121]
	s_barrier
	s_add_i32 s64, 0, 0x18000
	v_add_u32_e32 v2, s64, v153
	s_add_i32 s65, 0, 0x1c000
	ds_read_b128 v[158:161], v2
	ds_read_b128 v[162:165], v2 offset:1024
	ds_read_b128 v[166:169], v2 offset:2048
	ds_read_b128 v[170:173], v2 offset:3072
	v_add_u32_e32 v2, s65, v153
	ds_read_b128 v[174:177], v2
	ds_read_b128 v[178:181], v2 offset:1024
	ds_read_b128 v[182:185], v2 offset:2048
	ds_read_b128 v[186:189], v2 offset:3072
	s_add_u32 s34, s34, 0xb0000
	s_addc_u32 s35, s35, 0
	s_mov_b32 m0, s53
	v_lshl_add_u64 v[234:235], s[34:35], 0, v[140:141]
	ds_read_b128 v[190:193], v155 offset:32768
	ds_read_b128 v[194:197], v155 offset:33792
	ds_read_b128 v[202:205], v155 offset:34816
	ds_read_b128 v[206:209], v155 offset:35840
	ds_read_b128 v[210:213], v155 offset:36864
	ds_read_b128 v[214:217], v155 offset:37888
	ds_read_b128 v[218:221], v155 offset:38912
	ds_read_b128 v[222:225], v155 offset:39936
	global_load_lds_dwordx4 v[234:235], off
	v_lshl_add_u64 v[234:235], s[34:35], 0, v[136:137]
	s_mov_b32 m0, s54
	s_nop 0
	global_load_lds_dwordx4 v[234:235], off
	s_waitcnt vmcnt(8)
	s_waitcnt lgkmcnt(0)
	s_barrier
	s_waitcnt lgkmcnt(0)
	v_mfma_f32_16x16x32_bf16 v[90:93], v[158:161], v[190:193], v[90:93]
	v_mfma_f32_16x16x32_bf16 v[18:21], v[166:169], v[190:193], v[18:21]
	v_mfma_f32_16x16x32_bf16 v[6:9], v[158:161], v[202:205], v[6:9]
	v_mfma_f32_16x16x32_bf16 v[22:25], v[166:169], v[202:205], v[22:25]
	v_mfma_f32_16x16x32_bf16 v[10:13], v[158:161], v[210:213], v[10:13]
	v_mfma_f32_16x16x32_bf16 v[26:29], v[166:169], v[210:213], v[26:29]
	v_mfma_f32_16x16x32_bf16 v[14:17], v[158:161], v[218:221], v[14:17]
	v_mfma_f32_16x16x32_bf16 v[30:33], v[166:169], v[218:221], v[30:33]
	v_mfma_f32_16x16x32_bf16 v[90:93], v[162:165], v[194:197], v[90:93]
	v_mfma_f32_16x16x32_bf16 v[18:21], v[170:173], v[194:197], v[18:21]
	v_mfma_f32_16x16x32_bf16 v[6:9], v[162:165], v[206:209], v[6:9]
	v_mfma_f32_16x16x32_bf16 v[22:25], v[170:173], v[206:209], v[22:25]
	v_mfma_f32_16x16x32_bf16 v[10:13], v[162:165], v[214:217], v[10:13]
	v_mfma_f32_16x16x32_bf16 v[26:29], v[170:173], v[214:217], v[26:29]
	v_mfma_f32_16x16x32_bf16 v[14:17], v[162:165], v[222:225], v[14:17]
	v_mfma_f32_16x16x32_bf16 v[30:33], v[170:173], v[222:225], v[30:33]
	v_mfma_f32_16x16x32_bf16 v[34:37], v[174:177], v[190:193], v[34:37]
	v_mfma_f32_16x16x32_bf16 v[50:53], v[182:185], v[190:193], v[50:53]
	v_mfma_f32_16x16x32_bf16 v[38:41], v[174:177], v[202:205], v[38:41]
	v_mfma_f32_16x16x32_bf16 v[54:57], v[182:185], v[202:205], v[54:57]
	v_mfma_f32_16x16x32_bf16 v[42:45], v[174:177], v[210:213], v[42:45]
	v_mfma_f32_16x16x32_bf16 v[62:65], v[182:185], v[210:213], v[62:65]
	v_mfma_f32_16x16x32_bf16 v[46:49], v[174:177], v[218:221], v[46:49]
	v_mfma_f32_16x16x32_bf16 v[70:73], v[182:185], v[218:221], v[70:73]
	v_mfma_f32_16x16x32_bf16 v[34:37], v[178:181], v[194:197], v[34:37]
	v_mfma_f32_16x16x32_bf16 v[50:53], v[186:189], v[194:197], v[50:53]
	v_mfma_f32_16x16x32_bf16 v[38:41], v[178:181], v[206:209], v[38:41]
	v_mfma_f32_16x16x32_bf16 v[54:57], v[186:189], v[206:209], v[54:57]
	v_mfma_f32_16x16x32_bf16 v[42:45], v[178:181], v[214:217], v[42:45]
	v_mfma_f32_16x16x32_bf16 v[62:65], v[186:189], v[214:217], v[62:65]
	v_mfma_f32_16x16x32_bf16 v[46:49], v[178:181], v[222:225], v[46:49]
	v_mfma_f32_16x16x32_bf16 v[70:73], v[186:189], v[222:225], v[70:73]
	s_barrier
; #define PG8_STAGE_A(bufoff, base_, nx_, kb_, h_) do { if (GATHER) { if (nx_) PG8_STAGE_G(bufoff, kb_, goN, h_); else PG8_STAGE_G(bufoff, kb_, goC, h_); } \
;         else PG8_STAGE(bufoff, (base_) + (kb_) + (h_) * hstep, voffA); } while (0)
; #define PG8_STAGE(bufoff, gbase, voff) do { _Pragma("unroll") for (int _i = 0; _i < 2; ++_i) \
;         __builtin_amdgcn_global_load_lds((const unsigned*)((const char*)(gbase) + (voff)[_i]), (LAS unsigned*)(lds + (bufoff) + ldsw + _i * 8192), 16, 0, 0); } while (0)
; #define PG8_LDA(dst, b, h) do { _Pragma("unroll") for (int m = 0; m < 4; ++m) _Pragma("unroll") for (int k = 0; k < 2; ++k) dst[m][k] = *(const LAS bf16x8*)(lds + PG8_SA(b, h) + aoff + m * 2048 + k * 1024); } while (0)
; #define PG8_MMA(ai, bj, At, Bt) do { __builtin_amdgcn_s_setprio(1); _Pragma("unroll") for (int m = 0; m < 4; ++m) _Pragma("unroll") for (int n = 0; n < 2; ++n) _Pragma("unroll") for (int k = 0; k < 2; ++k) \
;         acc[ai][bj][m][n] = __builtin_amdgcn_mfma_f32_16x16x32_bf16(Bt[n][k], At[m][k], acc[ai][bj][m][n], 0, 0, 0); __builtin_amdgcn_s_setprio(0); } while (0)
; #define PG8_WAIT_V(n) asm volatile("s_waitcnt vmcnt(" #n ")" ::: "memory")
; #define PG8_WAIT_L(n) asm volatile("s_waitcnt lgkmcnt(" #n ")" ::: "memory")
; #define PG8_BAR __builtin_amdgcn_s_barrier()
; #define PG8_SCHED __builtin_amdgcn_sched_barrier(0)
; template <class Epi, class Sched, bool GATHER = false>
; __device__ __forceinline__ void gemm_phase(LAS unsigned char* lds, const Gemm g, const Sched& S, const Epi& E, const int tid) {
;     ...
;             PG8_LDA(At, 1, 1); PG8_STAGE(PG8_SB(1, 0), b3, voffB); PG8_STAGE(PG8_SB(1, 1), b3 + hstep, voffB); PG8_STAGE_A(PG8_SA(1, 0), (last ? nA : cA), last, kb3, 0);
;             PG8_WAIT_V(8); PG8_WAIT_L(0); PG8_BAR; PG8_MMA(1, 0, At, B0); PG8_MMA(1, 1, At, B1); PG8_BAR; PG8_SCHED;
;     ...
;         }
;         if (wr == 0) PG8_BAR;
	s_add_i32 s34, s64, s48
	v_lshl_add_u64 v[226:227], v[226:227], 0, s[0:1]
	s_mov_b32 m0, s34
	ds_read_b128 v[190:193], v155 offset:49152
	ds_read_b128 v[194:197], v155 offset:50176
	ds_read_b128 v[202:205], v155 offset:51200
	ds_read_b128 v[206:209], v155 offset:52224
	ds_read_b128 v[210:213], v155 offset:53248
	ds_read_b128 v[214:217], v155 offset:54272
	ds_read_b128 v[218:221], v155 offset:55296
	ds_read_b128 v[222:225], v155 offset:56320
	global_load_lds_dwordx4 v[226:227], off
	v_lshl_add_u64 v[226:227], v[228:229], 0, s[0:1]
	s_add_i32 m0, s34, 0x2000
	v_lshl_add_u64 v[198:199], v[198:199], 0, s[76:77]
	s_add_i32 s34, s65, s48
	global_load_lds_dwordx4 v[226:227], off
	v_lshl_add_u64 v[226:227], v[198:199], 0, v[138:139]
	s_mov_b32 m0, s34
	v_lshl_add_u64 v[198:199], v[198:199], 0, v[134:135]
	global_load_lds_dwordx4 v[226:227], off
	s_add_i32 m0, s34, 0x2000
	s_nop 0
	global_load_lds_dwordx4 v[198:199], off
	v_lshl_add_u64 v[198:199], v[230:231], 0, s[0:1]
	s_mov_b32 m0, s55
	s_nop 0
	global_load_lds_dwordx4 v[198:199], off
	v_lshl_add_u64 v[198:199], v[232:233], 0, s[0:1]
	s_mov_b32 m0, s56
	s_nop 0
	global_load_lds_dwordx4 v[198:199], off
	s_waitcnt vmcnt(8)
	s_waitcnt lgkmcnt(0)
	s_barrier
	s_waitcnt lgkmcnt(0)
	v_mfma_f32_16x16x32_bf16 v[58:61], v[158:161], v[190:193], v[58:61]
	v_mfma_f32_16x16x32_bf16 v[78:81], v[166:169], v[190:193], v[78:81]
	v_mfma_f32_16x16x32_bf16 v[66:69], v[158:161], v[202:205], v[66:69]
	v_mfma_f32_16x16x32_bf16 v[82:85], v[166:169], v[202:205], v[82:85]
	v_mfma_f32_16x16x32_bf16 v[74:77], v[158:161], v[210:213], v[74:77]
	v_mfma_f32_16x16x32_bf16 v[86:89], v[166:169], v[210:213], v[86:89]
	v_mfma_f32_16x16x32_bf16 v[94:97], v[158:161], v[218:221], v[94:97]
	v_mfma_f32_16x16x32_bf16 v[98:101], v[166:169], v[218:221], v[98:101]
	v_mfma_f32_16x16x32_bf16 v[58:61], v[162:165], v[194:197], v[58:61]
	v_mfma_f32_16x16x32_bf16 v[78:81], v[170:173], v[194:197], v[78:81]
	v_mfma_f32_16x16x32_bf16 v[66:69], v[162:165], v[206:209], v[66:69]
	v_mfma_f32_16x16x32_bf16 v[82:85], v[170:173], v[206:209], v[82:85]
	v_mfma_f32_16x16x32_bf16 v[74:77], v[162:165], v[214:217], v[74:77]
	v_mfma_f32_16x16x32_bf16 v[86:89], v[170:173], v[214:217], v[86:89]
	v_mfma_f32_16x16x32_bf16 v[94:97], v[162:165], v[222:225], v[94:97]
	v_mfma_f32_16x16x32_bf16 v[98:101], v[170:173], v[222:225], v[98:101]
	v_mfma_f32_16x16x32_bf16 v[114:117], v[174:177], v[190:193], v[114:117]
	v_mfma_f32_16x16x32_bf16 v[130:133], v[182:185], v[190:193], v[130:133]
	v_mfma_f32_16x16x32_bf16 v[110:113], v[174:177], v[202:205], v[110:113]
	v_mfma_f32_16x16x32_bf16 v[126:129], v[182:185], v[202:205], v[126:129]
	v_mfma_f32_16x16x32_bf16 v[106:109], v[174:177], v[210:213], v[106:109]
	v_mfma_f32_16x16x32_bf16 v[122:125], v[182:185], v[210:213], v[122:125]
	v_mfma_f32_16x16x32_bf16 v[102:105], v[174:177], v[218:221], v[102:105]
	v_mfma_f32_16x16x32_bf16 v[118:121], v[182:185], v[218:221], v[118:121]
	v_mfma_f32_16x16x32_bf16 v[114:117], v[178:181], v[194:197], v[114:117]
	v_mfma_f32_16x16x32_bf16 v[130:133], v[186:189], v[194:197], v[130:133]
	v_mfma_f32_16x16x32_bf16 v[110:113], v[178:181], v[206:209], v[110:113]
	v_mfma_f32_16x16x32_bf16 v[126:129], v[186:189], v[206:209], v[126:129]
	v_mfma_f32_16x16x32_bf16 v[106:109], v[178:181], v[214:217], v[106:109]
	v_mfma_f32_16x16x32_bf16 v[122:125], v[186:189], v[214:217], v[122:125]
	v_mfma_f32_16x16x32_bf16 v[102:105], v[178:181], v[222:225], v[102:105]
	v_mfma_f32_16x16x32_bf16 v[118:121], v[186:189], v[222:225], v[118:121]
	s_barrier
	s_add_i32 s63, s63, 2
	s_cmp_gt_u32 s63, 41
	s_mov_b64 s[34:35], s[30:31]
	s_cbranch_scc0 .LBB0_1505
	s_and_b64 vcc, exec, s[24:25]
	s_cbranch_vccz .LBB0_1508
	s_barrier
